# GEMM k-loops: back-edge rotated (loop-back barrier becomes the loop head) and segment-head scalar work hoisted above the barrier that opens each load segment
# baseline (speedup 1.0000x reference)
.LBB0_417:
	s_ashr_i32 s25, s24, 31
	s_lshl_b64 s[36:37], s[24:25], 21
	s_add_u32 s36, s48, s36
	s_addc_u32 s37, s49, s37
	s_and_b64 s[44:45], s[2:3], exec
	s_cselect_b32 s5, s37, s35
	s_cselect_b32 s7, s36, s34
	s_ashr_i32 s15, s14, 31
	s_lshl_b64 s[44:45], s[14:15], 21
	v_readlane_b32 s16, v254, 42
	v_readlane_b32 s17, v254, 43
	s_add_u32 s64, s16, s44
	s_addc_u32 s65, s17, s45
	s_and_b64 s[44:45], s[2:3], exec
	s_cselect_b32 s15, s65, s43
	s_cselect_b32 s25, s64, s42
	s_add_u32 s34, s34, 0x100080
	s_addc_u32 s35, s35, 0
	s_add_u32 s63, s42, 0x100
	v_mov_b32_e32 v2, 0
	s_addc_u32 s66, s43, 0
	s_mov_b32 s67, -2
	v_mov_b32_e32 v3, v2
	v_mov_b32_e32 v4, v2
	v_mov_b32_e32 v5, v2
	v_mov_b32_e32 v6, v2
	v_mov_b32_e32 v7, v2
	v_mov_b32_e32 v8, v2
	v_mov_b32_e32 v9, v2
	v_mov_b32_e32 v18, v2
	v_mov_b32_e32 v19, v2
	v_mov_b32_e32 v20, v2
	v_mov_b32_e32 v21, v2
	v_mov_b32_e32 v22, v2
	v_mov_b32_e32 v23, v2
	v_mov_b32_e32 v24, v2
	v_mov_b32_e32 v25, v2
	v_mov_b32_e32 v34, v2
	v_mov_b32_e32 v35, v2
	v_mov_b32_e32 v36, v2
	v_mov_b32_e32 v37, v2
	v_mov_b32_e32 v38, v2
	v_mov_b32_e32 v39, v2
	v_mov_b32_e32 v40, v2
	v_mov_b32_e32 v41, v2
	v_mov_b32_e32 v50, v2
	v_mov_b32_e32 v51, v2
	v_mov_b32_e32 v52, v2
	v_mov_b32_e32 v53, v2
	v_mov_b32_e32 v54, v2
	v_mov_b32_e32 v55, v2
	v_mov_b32_e32 v56, v2
	v_mov_b32_e32 v57, v2
	v_mov_b32_e32 v10, v2
	v_mov_b32_e32 v11, v2
	v_mov_b32_e32 v12, v2
	v_mov_b32_e32 v13, v2
	v_mov_b32_e32 v14, v2
	v_mov_b32_e32 v15, v2
	v_mov_b32_e32 v16, v2
	v_mov_b32_e32 v17, v2
	v_mov_b32_e32 v26, v2
	v_mov_b32_e32 v27, v2
	v_mov_b32_e32 v28, v2
	v_mov_b32_e32 v29, v2
	v_mov_b32_e32 v30, v2
	v_mov_b32_e32 v31, v2
	v_mov_b32_e32 v32, v2
	v_mov_b32_e32 v33, v2
	v_mov_b32_e32 v42, v2
	v_mov_b32_e32 v43, v2
	v_mov_b32_e32 v44, v2
	v_mov_b32_e32 v45, v2
	v_mov_b32_e32 v46, v2
	v_mov_b32_e32 v47, v2
	v_mov_b32_e32 v48, v2
	v_mov_b32_e32 v49, v2
	v_mov_b32_e32 v58, v2
	v_mov_b32_e32 v59, v2
	v_mov_b32_e32 v60, v2
	v_mov_b32_e32 v61, v2
	v_mov_b32_e32 v62, v2
	v_mov_b32_e32 v63, v2
	v_mov_b32_e32 v64, v2
	v_mov_b32_e32 v65, v2
	v_mov_b32_e32 v66, v2
	v_mov_b32_e32 v67, v2
	v_mov_b32_e32 v68, v2
	v_mov_b32_e32 v69, v2
	v_mov_b32_e32 v70, v2
	v_mov_b32_e32 v71, v2
	v_mov_b32_e32 v72, v2
	v_mov_b32_e32 v73, v2
	v_mov_b32_e32 v82, v2
	v_mov_b32_e32 v83, v2
	v_mov_b32_e32 v84, v2
	v_mov_b32_e32 v85, v2
	v_mov_b32_e32 v86, v2
	v_mov_b32_e32 v87, v2
	v_mov_b32_e32 v88, v2
	v_mov_b32_e32 v89, v2
	v_mov_b32_e32 v98, v2
	v_mov_b32_e32 v99, v2
	v_mov_b32_e32 v100, v2
	v_mov_b32_e32 v101, v2
	v_mov_b32_e32 v102, v2
	v_mov_b32_e32 v103, v2
	v_mov_b32_e32 v104, v2
	v_mov_b32_e32 v105, v2
	v_mov_b32_e32 v114, v2
	v_mov_b32_e32 v115, v2
	v_mov_b32_e32 v116, v2
	v_mov_b32_e32 v117, v2
	v_mov_b32_e32 v118, v2
	v_mov_b32_e32 v119, v2
	v_mov_b32_e32 v120, v2
	v_mov_b32_e32 v121, v2
	v_mov_b32_e32 v74, v2
	v_mov_b32_e32 v75, v2
	v_mov_b32_e32 v76, v2
	v_mov_b32_e32 v77, v2
	v_mov_b32_e32 v78, v2
	v_mov_b32_e32 v79, v2
	v_mov_b32_e32 v80, v2
	v_mov_b32_e32 v81, v2
	v_mov_b32_e32 v90, v2
	v_mov_b32_e32 v91, v2
	v_mov_b32_e32 v92, v2
	v_mov_b32_e32 v93, v2
	v_mov_b32_e32 v94, v2
	v_mov_b32_e32 v95, v2
	v_mov_b32_e32 v96, v2
	v_mov_b32_e32 v97, v2
	v_mov_b32_e32 v106, v2
	v_mov_b32_e32 v107, v2
	v_mov_b32_e32 v108, v2
	v_mov_b32_e32 v109, v2
	v_mov_b32_e32 v110, v2
	v_mov_b32_e32 v111, v2
	v_mov_b32_e32 v112, v2
	v_mov_b32_e32 v113, v2
	v_mov_b32_e32 v122, v2
	v_mov_b32_e32 v123, v2
	v_mov_b32_e32 v124, v2
	v_mov_b32_e32 v125, v2
	v_mov_b32_e32 v126, v2
	v_mov_b32_e32 v127, v2
	v_mov_b32_e32 v128, v2
	v_mov_b32_e32 v129, v2
	s_add_u32 s38, s34, 0xfff00080
	s_addc_u32 s39, s35, -1
	s_cmp_eq_u32 s67, 60
	s_cselect_b32 s45, s5, s39
	s_cselect_b32 s44, s7, s38
	s_cselect_b32 s43, s15, s66
	s_cselect_b32 s42, s25, s63
	s_add_i32 m0, s46, 0xc000
	s_branch .Lrot_P2a_body

.Lrot_P2a_body:
.LBB0_418:
	ds_read_b128 v[148:151], v168
	ds_read_b128 v[152:155], v168 offset:1024
	ds_read_b128 v[172:175], v168 offset:2048
	ds_read_b128 v[176:179], v168 offset:3072
	ds_read_b128 v[186:189], v169
	ds_read_b128 v[190:193], v169 offset:1024
	ds_read_b128 v[194:197], v169 offset:2048
	ds_read_b128 v[198:201], v169 offset:3072
	ds_read_b128 v[202:205], v170
	ds_read_b128 v[206:209], v170 offset:1024
	ds_read_b128 v[210:213], v170 offset:2048
	ds_read_b128 v[214:217], v170 offset:3072
	ds_read_b128 v[218:221], v170 offset:4096
	ds_read_b128 v[222:225], v170 offset:5120
	ds_read_b128 v[226:229], v170 offset:6144
	ds_read_b128 v[230:233], v170 offset:7168
	global_load_lds_dwordx4 v140, s[34:35]
	s_add_i32 m0, s46, 0xe000
	s_nop 0
	global_load_lds_dwordx4 v142, s[34:35]
	s_waitcnt vmcnt(8)
	s_waitcnt lgkmcnt(0)
	s_barrier
	s_setprio 1
	s_waitcnt lgkmcnt(0)
	v_mfma_f32_16x16x32_f16 v[126:129], v[148:151], v[202:205], v[126:129]
	v_mfma_f32_16x16x32_f16 v[122:125], v[172:175], v[202:205], v[122:125]
	v_mfma_f32_16x16x32_f16 v[110:113], v[148:151], v[210:213], v[110:113]
	v_mfma_f32_16x16x32_f16 v[106:109], v[172:175], v[210:213], v[106:109]
	v_mfma_f32_16x16x32_f16 v[94:97], v[148:151], v[218:221], v[94:97]
	v_mfma_f32_16x16x32_f16 v[90:93], v[172:175], v[218:221], v[90:93]
	v_mfma_f32_16x16x32_f16 v[78:81], v[148:151], v[226:229], v[78:81]
	v_mfma_f32_16x16x32_f16 v[74:77], v[172:175], v[226:229], v[74:77]
	v_mfma_f32_16x16x32_f16 v[126:129], v[152:155], v[206:209], v[126:129]
	v_mfma_f32_16x16x32_f16 v[122:125], v[176:179], v[206:209], v[122:125]
	v_mfma_f32_16x16x32_f16 v[110:113], v[152:155], v[214:217], v[110:113]
	v_mfma_f32_16x16x32_f16 v[106:109], v[176:179], v[214:217], v[106:109]
	v_mfma_f32_16x16x32_f16 v[94:97], v[152:155], v[222:225], v[94:97]
	v_mfma_f32_16x16x32_f16 v[90:93], v[176:179], v[222:225], v[90:93]
	v_mfma_f32_16x16x32_f16 v[78:81], v[152:155], v[230:233], v[78:81]
	v_mfma_f32_16x16x32_f16 v[74:77], v[176:179], v[230:233], v[74:77]
	s_setprio 0
	s_setprio 1
	v_mfma_f32_16x16x32_f16 v[118:121], v[186:189], v[202:205], v[118:121]
	v_mfma_f32_16x16x32_f16 v[114:117], v[194:197], v[202:205], v[114:117]
	v_mfma_f32_16x16x32_f16 v[102:105], v[186:189], v[210:213], v[102:105]
	v_mfma_f32_16x16x32_f16 v[98:101], v[194:197], v[210:213], v[98:101]
	v_mfma_f32_16x16x32_f16 v[86:89], v[186:189], v[218:221], v[86:89]
	v_mfma_f32_16x16x32_f16 v[82:85], v[194:197], v[218:221], v[82:85]
	v_mfma_f32_16x16x32_f16 v[70:73], v[186:189], v[226:229], v[70:73]
	v_mfma_f32_16x16x32_f16 v[66:69], v[194:197], v[226:229], v[66:69]
	v_mfma_f32_16x16x32_f16 v[118:121], v[190:193], v[206:209], v[118:121]
	v_mfma_f32_16x16x32_f16 v[114:117], v[198:201], v[206:209], v[114:117]
	v_mfma_f32_16x16x32_f16 v[102:105], v[190:193], v[214:217], v[102:105]
	v_mfma_f32_16x16x32_f16 v[98:101], v[198:201], v[214:217], v[98:101]
	v_mfma_f32_16x16x32_f16 v[86:89], v[190:193], v[222:225], v[86:89]
	v_mfma_f32_16x16x32_f16 v[82:85], v[198:201], v[222:225], v[82:85]
	v_mfma_f32_16x16x32_f16 v[70:73], v[190:193], v[230:233], v[70:73]
	v_mfma_f32_16x16x32_f16 v[66:69], v[198:201], v[230:233], v[66:69]
	s_setprio 0
	s_add_u32 s98, s42, s10
	s_addc_u32 s99, s43, s11
	s_add_u32 s100, s44, s10
	s_addc_u32 s101, s45, s11
	s_add_i32 s38, s61, s33
	s_mov_b32 m0, s38
	s_barrier
	ds_read_b128 v[202:205], v170 offset:16384
	ds_read_b128 v[206:209], v170 offset:17408
	ds_read_b128 v[210:213], v170 offset:18432
	ds_read_b128 v[214:217], v170 offset:19456
	ds_read_b128 v[218:221], v170 offset:20480
	ds_read_b128 v[222:225], v170 offset:21504
	ds_read_b128 v[226:229], v170 offset:22528
	ds_read_b128 v[230:233], v170 offset:23552
	global_load_lds_dwordx4 v132, s[42:43]
	s_add_i32 m0, s38, 0x2000
	s_add_u32 s72, s42, 0x100000
	s_addc_u32 s73, s43, 0
	s_add_i32 s38, s62, s33
	global_load_lds_dwordx4 v136, s[42:43]
	s_mov_b32 m0, s38
	s_nop 0
	global_load_lds_dwordx4 v132, s[72:73]
	s_add_i32 m0, s38, 0x2000
	s_nop 0
	global_load_lds_dwordx4 v136, s[72:73]
	s_mov_b32 m0, s46
	s_nop 0
	global_load_lds_dwordx4 v130, s[44:45]
	s_mov_b32 m0, s47
	s_nop 0
	global_load_lds_dwordx4 v134, s[44:45]
	s_waitcnt vmcnt(8)
	s_waitcnt lgkmcnt(0)
	s_barrier
	s_setprio 1
	s_waitcnt lgkmcnt(0)
	v_mfma_f32_16x16x32_f16 v[62:65], v[148:151], v[202:205], v[62:65]
	v_mfma_f32_16x16x32_f16 v[58:61], v[172:175], v[202:205], v[58:61]
	v_mfma_f32_16x16x32_f16 v[46:49], v[148:151], v[210:213], v[46:49]
	v_mfma_f32_16x16x32_f16 v[42:45], v[172:175], v[210:213], v[42:45]
	v_mfma_f32_16x16x32_f16 v[30:33], v[148:151], v[218:221], v[30:33]
	v_mfma_f32_16x16x32_f16 v[26:29], v[172:175], v[218:221], v[26:29]
	v_mfma_f32_16x16x32_f16 v[14:17], v[148:151], v[226:229], v[14:17]
	v_mfma_f32_16x16x32_f16 v[10:13], v[172:175], v[226:229], v[10:13]
	v_mfma_f32_16x16x32_f16 v[62:65], v[152:155], v[206:209], v[62:65]
	v_mfma_f32_16x16x32_f16 v[58:61], v[176:179], v[206:209], v[58:61]
	v_mfma_f32_16x16x32_f16 v[46:49], v[152:155], v[214:217], v[46:49]
	v_mfma_f32_16x16x32_f16 v[42:45], v[176:179], v[214:217], v[42:45]
	v_mfma_f32_16x16x32_f16 v[30:33], v[152:155], v[222:225], v[30:33]
	v_mfma_f32_16x16x32_f16 v[26:29], v[176:179], v[222:225], v[26:29]
	v_mfma_f32_16x16x32_f16 v[14:17], v[152:155], v[230:233], v[14:17]
	v_mfma_f32_16x16x32_f16 v[10:13], v[176:179], v[230:233], v[10:13]
	s_setprio 0
	s_setprio 1
	v_mfma_f32_16x16x32_f16 v[54:57], v[186:189], v[202:205], v[54:57]
	v_mfma_f32_16x16x32_f16 v[50:53], v[194:197], v[202:205], v[50:53]
	v_mfma_f32_16x16x32_f16 v[38:41], v[186:189], v[210:213], v[38:41]
	v_mfma_f32_16x16x32_f16 v[34:37], v[194:197], v[210:213], v[34:37]
	v_mfma_f32_16x16x32_f16 v[22:25], v[186:189], v[218:221], v[22:25]
	v_mfma_f32_16x16x32_f16 v[18:21], v[194:197], v[218:221], v[18:21]
	v_mfma_f32_16x16x32_f16 v[6:9], v[186:189], v[226:229], v[6:9]
	v_mfma_f32_16x16x32_f16 v[2:5], v[194:197], v[226:229], v[2:5]
	v_mfma_f32_16x16x32_f16 v[54:57], v[190:193], v[206:209], v[54:57]
	v_mfma_f32_16x16x32_f16 v[50:53], v[198:201], v[206:209], v[50:53]
	v_mfma_f32_16x16x32_f16 v[38:41], v[190:193], v[214:217], v[38:41]
	v_mfma_f32_16x16x32_f16 v[34:37], v[198:201], v[214:217], v[34:37]
	v_mfma_f32_16x16x32_f16 v[22:25], v[190:193], v[222:225], v[22:25]
	v_mfma_f32_16x16x32_f16 v[18:21], v[198:201], v[222:225], v[18:21]
	v_mfma_f32_16x16x32_f16 v[6:9], v[190:193], v[230:233], v[6:9]
	v_mfma_f32_16x16x32_f16 v[2:5], v[198:201], v[230:233], v[2:5]
	s_setprio 0
	s_add_i32 s38, 0, 0x18000
	s_add_i32 s39, 0, 0x1c000
	s_add_u32 s44, s44, 0x100000
	s_addc_u32 s45, s45, 0
	s_mov_b32 m0, s50
	s_barrier
	v_add_u32_e32 v138, s38, v164
	ds_read_b128 v[148:151], v138
	ds_read_b128 v[152:155], v138 offset:1024
	ds_read_b128 v[172:175], v138 offset:2048
	ds_read_b128 v[176:179], v138 offset:3072
	v_add_u32_e32 v138, s39, v164
	ds_read_b128 v[186:189], v138
	ds_read_b128 v[190:193], v138 offset:1024
	ds_read_b128 v[194:197], v138 offset:2048
	ds_read_b128 v[198:201], v138 offset:3072
	ds_read_b128 v[202:205], v170 offset:32768
	ds_read_b128 v[206:209], v170 offset:33792
	ds_read_b128 v[210:213], v170 offset:34816
	ds_read_b128 v[214:217], v170 offset:35840
	ds_read_b128 v[218:221], v170 offset:36864
	ds_read_b128 v[222:225], v170 offset:37888
	ds_read_b128 v[226:229], v170 offset:38912
	ds_read_b128 v[230:233], v170 offset:39936
	global_load_lds_dwordx4 v130, s[44:45]
	s_mov_b32 m0, s51
	s_nop 0
	global_load_lds_dwordx4 v134, s[44:45]
	s_waitcnt vmcnt(8)
	s_waitcnt lgkmcnt(0)
	s_barrier
	s_setprio 1
	s_waitcnt lgkmcnt(0)
	v_mfma_f32_16x16x32_f16 v[126:129], v[148:151], v[202:205], v[126:129]
	v_mfma_f32_16x16x32_f16 v[122:125], v[172:175], v[202:205], v[122:125]
	v_mfma_f32_16x16x32_f16 v[110:113], v[148:151], v[210:213], v[110:113]
	v_mfma_f32_16x16x32_f16 v[106:109], v[172:175], v[210:213], v[106:109]
	v_mfma_f32_16x16x32_f16 v[94:97], v[148:151], v[218:221], v[94:97]
	v_mfma_f32_16x16x32_f16 v[90:93], v[172:175], v[218:221], v[90:93]
	v_mfma_f32_16x16x32_f16 v[78:81], v[148:151], v[226:229], v[78:81]
	v_mfma_f32_16x16x32_f16 v[74:77], v[172:175], v[226:229], v[74:77]
	v_mfma_f32_16x16x32_f16 v[126:129], v[152:155], v[206:209], v[126:129]
	v_mfma_f32_16x16x32_f16 v[122:125], v[176:179], v[206:209], v[122:125]
	v_mfma_f32_16x16x32_f16 v[110:113], v[152:155], v[214:217], v[110:113]
	v_mfma_f32_16x16x32_f16 v[106:109], v[176:179], v[214:217], v[106:109]
	v_mfma_f32_16x16x32_f16 v[94:97], v[152:155], v[222:225], v[94:97]
	v_mfma_f32_16x16x32_f16 v[90:93], v[176:179], v[222:225], v[90:93]
	v_mfma_f32_16x16x32_f16 v[78:81], v[152:155], v[230:233], v[78:81]
	v_mfma_f32_16x16x32_f16 v[74:77], v[176:179], v[230:233], v[74:77]
	s_setprio 0
	s_setprio 1
	v_mfma_f32_16x16x32_f16 v[118:121], v[186:189], v[202:205], v[118:121]
	v_mfma_f32_16x16x32_f16 v[114:117], v[194:197], v[202:205], v[114:117]
	v_mfma_f32_16x16x32_f16 v[102:105], v[186:189], v[210:213], v[102:105]
	v_mfma_f32_16x16x32_f16 v[98:101], v[194:197], v[210:213], v[98:101]
	v_mfma_f32_16x16x32_f16 v[86:89], v[186:189], v[218:221], v[86:89]
	v_mfma_f32_16x16x32_f16 v[82:85], v[194:197], v[218:221], v[82:85]
	v_mfma_f32_16x16x32_f16 v[70:73], v[186:189], v[226:229], v[70:73]
	v_mfma_f32_16x16x32_f16 v[66:69], v[194:197], v[226:229], v[66:69]
	v_mfma_f32_16x16x32_f16 v[118:121], v[190:193], v[206:209], v[118:121]
	v_mfma_f32_16x16x32_f16 v[114:117], v[198:201], v[206:209], v[114:117]
	v_mfma_f32_16x16x32_f16 v[102:105], v[190:193], v[214:217], v[102:105]
	v_mfma_f32_16x16x32_f16 v[98:101], v[198:201], v[214:217], v[98:101]
	v_mfma_f32_16x16x32_f16 v[86:89], v[190:193], v[222:225], v[86:89]
	v_mfma_f32_16x16x32_f16 v[82:85], v[198:201], v[222:225], v[82:85]
	v_mfma_f32_16x16x32_f16 v[70:73], v[190:193], v[230:233], v[70:73]
	v_mfma_f32_16x16x32_f16 v[66:69], v[198:201], v[230:233], v[66:69]
	s_setprio 0
	s_add_i32 s38, s38, s33
	s_mov_b32 m0, s38
	s_barrier
	ds_read_b128 v[202:205], v170 offset:49152
	ds_read_b128 v[206:209], v170 offset:50176
	ds_read_b128 v[210:213], v170 offset:51200
	ds_read_b128 v[214:217], v170 offset:52224
	ds_read_b128 v[218:221], v170 offset:53248
	ds_read_b128 v[222:225], v170 offset:54272
	ds_read_b128 v[226:229], v170 offset:55296
	ds_read_b128 v[230:233], v170 offset:56320
	global_load_lds_dwordx4 v132, s[98:99]
	s_add_i32 m0, s38, 0x2000
	s_add_u32 s42, s42, 0x100080
	s_addc_u32 s43, s43, 0
	s_add_i32 s38, s39, s33
	global_load_lds_dwordx4 v136, s[98:99]
	s_mov_b32 m0, s38
	s_nop 0
	global_load_lds_dwordx4 v132, s[42:43]
	s_add_i32 m0, s38, 0x2000
	s_nop 0
	global_load_lds_dwordx4 v136, s[42:43]
	s_mov_b32 m0, s53
	s_nop 0
	global_load_lds_dwordx4 v130, s[100:101]
	s_mov_b32 m0, s58
	s_nop 0
	global_load_lds_dwordx4 v134, s[100:101]
	s_waitcnt vmcnt(8)
	s_waitcnt lgkmcnt(0)
	s_barrier
	s_setprio 1
	s_waitcnt lgkmcnt(0)
	v_mfma_f32_16x16x32_f16 v[62:65], v[148:151], v[202:205], v[62:65]
	v_mfma_f32_16x16x32_f16 v[58:61], v[172:175], v[202:205], v[58:61]
	v_mfma_f32_16x16x32_f16 v[46:49], v[148:151], v[210:213], v[46:49]
	v_mfma_f32_16x16x32_f16 v[42:45], v[172:175], v[210:213], v[42:45]
	v_mfma_f32_16x16x32_f16 v[30:33], v[148:151], v[218:221], v[30:33]
	v_mfma_f32_16x16x32_f16 v[26:29], v[172:175], v[218:221], v[26:29]
	v_mfma_f32_16x16x32_f16 v[14:17], v[148:151], v[226:229], v[14:17]
	v_mfma_f32_16x16x32_f16 v[10:13], v[172:175], v[226:229], v[10:13]
	v_mfma_f32_16x16x32_f16 v[62:65], v[152:155], v[206:209], v[62:65]
	v_mfma_f32_16x16x32_f16 v[58:61], v[176:179], v[206:209], v[58:61]
	v_mfma_f32_16x16x32_f16 v[46:49], v[152:155], v[214:217], v[46:49]
	v_mfma_f32_16x16x32_f16 v[42:45], v[176:179], v[214:217], v[42:45]
	v_mfma_f32_16x16x32_f16 v[30:33], v[152:155], v[222:225], v[30:33]
	v_mfma_f32_16x16x32_f16 v[26:29], v[176:179], v[222:225], v[26:29]
	v_mfma_f32_16x16x32_f16 v[14:17], v[152:155], v[230:233], v[14:17]
	v_mfma_f32_16x16x32_f16 v[10:13], v[176:179], v[230:233], v[10:13]
	s_setprio 0
	s_setprio 1
	v_mfma_f32_16x16x32_f16 v[54:57], v[186:189], v[202:205], v[54:57]
	v_mfma_f32_16x16x32_f16 v[50:53], v[194:197], v[202:205], v[50:53]
	v_mfma_f32_16x16x32_f16 v[38:41], v[186:189], v[210:213], v[38:41]
	v_mfma_f32_16x16x32_f16 v[34:37], v[194:197], v[210:213], v[34:37]
	v_mfma_f32_16x16x32_f16 v[22:25], v[186:189], v[218:221], v[22:25]
	v_mfma_f32_16x16x32_f16 v[18:21], v[194:197], v[218:221], v[18:21]
	v_mfma_f32_16x16x32_f16 v[6:9], v[186:189], v[226:229], v[6:9]
	v_mfma_f32_16x16x32_f16 v[2:5], v[194:197], v[226:229], v[2:5]
	v_mfma_f32_16x16x32_f16 v[54:57], v[190:193], v[206:209], v[54:57]
	v_mfma_f32_16x16x32_f16 v[50:53], v[198:201], v[206:209], v[50:53]
	v_mfma_f32_16x16x32_f16 v[38:41], v[190:193], v[214:217], v[38:41]
	v_mfma_f32_16x16x32_f16 v[34:37], v[198:201], v[214:217], v[34:37]
	v_mfma_f32_16x16x32_f16 v[22:25], v[190:193], v[222:225], v[22:25]
	v_mfma_f32_16x16x32_f16 v[18:21], v[198:201], v[222:225], v[18:21]
	v_mfma_f32_16x16x32_f16 v[6:9], v[190:193], v[230:233], v[6:9]
	v_mfma_f32_16x16x32_f16 v[2:5], v[198:201], v[230:233], v[2:5]
	s_setprio 0
	s_add_i32 s67, s67, 2
	s_add_u32 s34, s34, 0x100
	s_addc_u32 s35, s35, 0
	s_add_u32 s63, s63, 0x100
	s_addc_u32 s66, s66, 0
	s_cmp_gt_u32 s67, 61
	s_cbranch_scc1 .Lrot_P2a_exit
	s_add_u32 s38, s34, 0xfff00080
	s_addc_u32 s39, s35, -1
	s_cmp_eq_u32 s67, 60
	s_cselect_b32 s45, s5, s39
	s_cselect_b32 s44, s7, s38
	s_cselect_b32 s43, s15, s66
	s_cselect_b32 s42, s25, s63
	s_add_i32 m0, s46, 0xc000
	s_branch .Lrot_P2a_head
.Lrot_P2a_exit:
	s_barrier
	s_and_b64 vcc, exec, s[12:13]
	s_cbranch_vccz .LBB0_421
	s_barrier

.LBB0_546:
	s_ashr_i32 s67, s66, 31
	s_lshl_b64 s[44:45], s[66:67], 20
	s_add_u32 s84, s96, s44
	s_addc_u32 s85, s97, s45
	s_and_b64 s[44:45], s[2:3], exec
	s_cselect_b32 s5, s85, s35
	s_cselect_b32 s7, s84, s34
	s_ashr_i32 s65, s64, 31
	s_lshl_b64 s[44:45], s[64:65], 20
	s_add_u32 s86, s33, s44
	s_addc_u32 s87, s46, s45
	s_and_b64 s[44:45], s[2:3], exec
	s_cselect_b32 s8, s87, s43
	s_cselect_b32 s65, s86, s42
	s_add_u32 s34, s34, 0x80080
	s_addc_u32 s35, s35, 0
	s_add_u32 s67, s42, 0x100
	v_mov_b32_e32 v2, 0
	s_addc_u32 s73, s43, 0
	s_mov_b32 s74, -2
	v_mov_b32_e32 v3, v2
	v_mov_b32_e32 v4, v2
	v_mov_b32_e32 v5, v2
	v_mov_b32_e32 v6, v2
	v_mov_b32_e32 v7, v2
	v_mov_b32_e32 v8, v2
	v_mov_b32_e32 v9, v2
	v_mov_b32_e32 v18, v2
	v_mov_b32_e32 v19, v2
	v_mov_b32_e32 v20, v2
	v_mov_b32_e32 v21, v2
	v_mov_b32_e32 v22, v2
	v_mov_b32_e32 v23, v2
	v_mov_b32_e32 v24, v2
	v_mov_b32_e32 v25, v2
	v_mov_b32_e32 v50, v2
	v_mov_b32_e32 v51, v2
	v_mov_b32_e32 v52, v2
	v_mov_b32_e32 v53, v2
	v_mov_b32_e32 v54, v2
	v_mov_b32_e32 v55, v2
	v_mov_b32_e32 v56, v2
	v_mov_b32_e32 v57, v2
	v_mov_b32_e32 v66, v2
	v_mov_b32_e32 v67, v2
	v_mov_b32_e32 v68, v2
	v_mov_b32_e32 v69, v2
	v_mov_b32_e32 v70, v2
	v_mov_b32_e32 v71, v2
	v_mov_b32_e32 v72, v2
	v_mov_b32_e32 v73, v2
	v_mov_b32_e32 v10, v2
	v_mov_b32_e32 v11, v2
	v_mov_b32_e32 v12, v2
	v_mov_b32_e32 v13, v2
	v_mov_b32_e32 v14, v2
	v_mov_b32_e32 v15, v2
	v_mov_b32_e32 v16, v2
	v_mov_b32_e32 v17, v2
	v_mov_b32_e32 v34, v2
	v_mov_b32_e32 v35, v2
	v_mov_b32_e32 v36, v2
	v_mov_b32_e32 v37, v2
	v_mov_b32_e32 v38, v2
	v_mov_b32_e32 v39, v2
	v_mov_b32_e32 v40, v2
	v_mov_b32_e32 v41, v2
	v_mov_b32_e32 v58, v2
	v_mov_b32_e32 v59, v2
	v_mov_b32_e32 v60, v2
	v_mov_b32_e32 v61, v2
	v_mov_b32_e32 v62, v2
	v_mov_b32_e32 v63, v2
	v_mov_b32_e32 v64, v2
	v_mov_b32_e32 v65, v2
	v_mov_b32_e32 v74, v2
	v_mov_b32_e32 v75, v2
	v_mov_b32_e32 v76, v2
	v_mov_b32_e32 v77, v2
	v_mov_b32_e32 v78, v2
	v_mov_b32_e32 v79, v2
	v_mov_b32_e32 v80, v2
	v_mov_b32_e32 v81, v2
	v_mov_b32_e32 v82, v2
	v_mov_b32_e32 v83, v2
	v_mov_b32_e32 v84, v2
	v_mov_b32_e32 v85, v2
	v_mov_b32_e32 v86, v2
	v_mov_b32_e32 v87, v2
	v_mov_b32_e32 v88, v2
	v_mov_b32_e32 v89, v2
	v_mov_b32_e32 v98, v2
	v_mov_b32_e32 v99, v2
	v_mov_b32_e32 v100, v2
	v_mov_b32_e32 v101, v2
	v_mov_b32_e32 v102, v2
	v_mov_b32_e32 v103, v2
	v_mov_b32_e32 v104, v2
	v_mov_b32_e32 v105, v2
	v_mov_b32_e32 v114, v2
	v_mov_b32_e32 v115, v2
	v_mov_b32_e32 v116, v2
	v_mov_b32_e32 v117, v2
	v_mov_b32_e32 v118, v2
	v_mov_b32_e32 v119, v2
	v_mov_b32_e32 v120, v2
	v_mov_b32_e32 v121, v2
	v_mov_b32_e32 v130, v2
	v_mov_b32_e32 v131, v2
	v_mov_b32_e32 v132, v2
	v_mov_b32_e32 v133, v2
	v_mov_b32_e32 v134, v2
	v_mov_b32_e32 v135, v2
	v_mov_b32_e32 v136, v2
	v_mov_b32_e32 v137, v2
	v_mov_b32_e32 v90, v2
	v_mov_b32_e32 v91, v2
	v_mov_b32_e32 v92, v2
	v_mov_b32_e32 v93, v2
	v_mov_b32_e32 v94, v2
	v_mov_b32_e32 v95, v2
	v_mov_b32_e32 v96, v2
	v_mov_b32_e32 v97, v2
	v_mov_b32_e32 v106, v2
	v_mov_b32_e32 v107, v2
	v_mov_b32_e32 v108, v2
	v_mov_b32_e32 v109, v2
	v_mov_b32_e32 v110, v2
	v_mov_b32_e32 v111, v2
	v_mov_b32_e32 v112, v2
	v_mov_b32_e32 v113, v2
	v_mov_b32_e32 v122, v2
	v_mov_b32_e32 v123, v2
	v_mov_b32_e32 v124, v2
	v_mov_b32_e32 v125, v2
	v_mov_b32_e32 v126, v2
	v_mov_b32_e32 v127, v2
	v_mov_b32_e32 v128, v2
	v_mov_b32_e32 v129, v2
	v_mov_b32_e32 v138, v2
	v_mov_b32_e32 v139, v2
	v_mov_b32_e32 v140, v2
	v_mov_b32_e32 v141, v2
	v_mov_b32_e32 v142, v2
	v_mov_b32_e32 v143, v2
	v_mov_b32_e32 v144, v2
	v_mov_b32_e32 v145, v2
	s_add_u32 s38, s34, 0xfff80080
	s_addc_u32 s39, s35, -1
	s_cmp_eq_u32 s74, 28
	s_cselect_b32 s45, s5, s39
	s_cselect_b32 s44, s7, s38
	s_cselect_b32 s43, s8, s73
	s_cselect_b32 s42, s65, s67
	s_add_i32 m0, s50, 0xc000
	s_branch .Lrot_P2b_body

.Lrot_P2b_body:
.LBB0_547:
	ds_read_b128 v[26:29], v191
	ds_read_b128 v[30:33], v191 offset:1024
	ds_read_b128 v[42:45], v191 offset:2048
	ds_read_b128 v[46:49], v191 offset:3072
	ds_read_b128 v[168:171], v192
	ds_read_b128 v[172:175], v192 offset:1024
	ds_read_b128 v[176:179], v192 offset:2048
	ds_read_b128 v[194:197], v192 offset:3072
	ds_read_b128 v[198:201], v193
	ds_read_b128 v[202:205], v193 offset:1024
	ds_read_b128 v[206:209], v193 offset:2048
	ds_read_b128 v[210:213], v193 offset:3072
	ds_read_b128 v[214:217], v193 offset:4096
	ds_read_b128 v[218:221], v193 offset:5120
	ds_read_b128 v[222:225], v193 offset:6144
	ds_read_b128 v[226:229], v193 offset:7168
	global_load_lds_dwordx4 v156, s[34:35]
	s_add_i32 m0, s50, 0xe000
	s_nop 0
	global_load_lds_dwordx4 v158, s[34:35]
	s_waitcnt vmcnt(8)
	s_waitcnt lgkmcnt(0)
	s_barrier
	s_setprio 1
	s_waitcnt lgkmcnt(0)
	v_mfma_i32_16x16x64_i8 v[142:145], v[26:29], v[198:201], v[142:145]
	v_mfma_i32_16x16x64_i8 v[138:141], v[42:45], v[198:201], v[138:141]
	v_mfma_i32_16x16x64_i8 v[126:129], v[26:29], v[206:209], v[126:129]
	v_mfma_i32_16x16x64_i8 v[122:125], v[42:45], v[206:209], v[122:125]
	v_mfma_i32_16x16x64_i8 v[110:113], v[26:29], v[214:217], v[110:113]
	v_mfma_i32_16x16x64_i8 v[106:109], v[42:45], v[214:217], v[106:109]
	v_mfma_i32_16x16x64_i8 v[94:97], v[26:29], v[222:225], v[94:97]
	v_mfma_i32_16x16x64_i8 v[90:93], v[42:45], v[222:225], v[90:93]
	v_mfma_i32_16x16x64_i8 v[142:145], v[30:33], v[202:205], v[142:145]
	v_mfma_i32_16x16x64_i8 v[138:141], v[46:49], v[202:205], v[138:141]
	v_mfma_i32_16x16x64_i8 v[126:129], v[30:33], v[210:213], v[126:129]
	v_mfma_i32_16x16x64_i8 v[122:125], v[46:49], v[210:213], v[122:125]
	v_mfma_i32_16x16x64_i8 v[110:113], v[30:33], v[218:221], v[110:113]
	v_mfma_i32_16x16x64_i8 v[106:109], v[46:49], v[218:221], v[106:109]
	v_mfma_i32_16x16x64_i8 v[94:97], v[30:33], v[226:229], v[94:97]
	v_mfma_i32_16x16x64_i8 v[90:93], v[46:49], v[226:229], v[90:93]
	s_setprio 0
	s_setprio 1
	v_mfma_i32_16x16x64_i8 v[134:137], v[168:171], v[198:201], v[134:137]
	v_mfma_i32_16x16x64_i8 v[130:133], v[176:179], v[198:201], v[130:133]
	v_mfma_i32_16x16x64_i8 v[118:121], v[168:171], v[206:209], v[118:121]
	v_mfma_i32_16x16x64_i8 v[114:117], v[176:179], v[206:209], v[114:117]
	v_mfma_i32_16x16x64_i8 v[102:105], v[168:171], v[214:217], v[102:105]
	v_mfma_i32_16x16x64_i8 v[98:101], v[176:179], v[214:217], v[98:101]
	v_mfma_i32_16x16x64_i8 v[86:89], v[168:171], v[222:225], v[86:89]
	v_mfma_i32_16x16x64_i8 v[82:85], v[176:179], v[222:225], v[82:85]
	v_mfma_i32_16x16x64_i8 v[134:137], v[172:175], v[202:205], v[134:137]
	v_mfma_i32_16x16x64_i8 v[130:133], v[194:197], v[202:205], v[130:133]
	v_mfma_i32_16x16x64_i8 v[118:121], v[172:175], v[210:213], v[118:121]
	v_mfma_i32_16x16x64_i8 v[114:117], v[194:197], v[210:213], v[114:117]
	v_mfma_i32_16x16x64_i8 v[102:105], v[172:175], v[218:221], v[102:105]
	v_mfma_i32_16x16x64_i8 v[98:101], v[194:197], v[218:221], v[98:101]
	v_mfma_i32_16x16x64_i8 v[86:89], v[172:175], v[226:229], v[86:89]
	v_mfma_i32_16x16x64_i8 v[82:85], v[194:197], v[226:229], v[82:85]
	s_setprio 0
	s_add_u32 s98, s42, s12
	s_addc_u32 s99, s43, s13
	s_add_u32 s100, s44, s12
	s_addc_u32 s101, s45, s13
	s_add_i32 s38, s62, s47
	s_mov_b32 m0, s38
	s_barrier
	ds_read_b128 v[198:201], v193 offset:16384
	ds_read_b128 v[202:205], v193 offset:17408
	ds_read_b128 v[206:209], v193 offset:18432
	ds_read_b128 v[210:213], v193 offset:19456
	ds_read_b128 v[214:217], v193 offset:20480
	ds_read_b128 v[218:221], v193 offset:21504
	ds_read_b128 v[222:225], v193 offset:22528
	ds_read_b128 v[226:229], v193 offset:23552
	global_load_lds_dwordx4 v148, s[42:43]
	s_add_i32 m0, s38, 0x2000
	s_add_u32 s76, s42, 0x80000
	s_addc_u32 s77, s43, 0
	s_add_i32 s38, s63, s47
	global_load_lds_dwordx4 v152, s[42:43]
	s_mov_b32 m0, s38
	s_nop 0
	global_load_lds_dwordx4 v148, s[76:77]
	s_add_i32 m0, s38, 0x2000
	s_nop 0
	global_load_lds_dwordx4 v152, s[76:77]
	s_mov_b32 m0, s50
	s_nop 0
	global_load_lds_dwordx4 v146, s[44:45]
	s_mov_b32 m0, s51
	s_nop 0
	global_load_lds_dwordx4 v150, s[44:45]
	s_waitcnt vmcnt(8)
	s_waitcnt lgkmcnt(0)
	s_barrier
	s_setprio 1
	s_waitcnt lgkmcnt(0)
	v_mfma_i32_16x16x64_i8 v[78:81], v[26:29], v[198:201], v[78:81]
	v_mfma_i32_16x16x64_i8 v[74:77], v[42:45], v[198:201], v[74:77]
	v_mfma_i32_16x16x64_i8 v[62:65], v[26:29], v[206:209], v[62:65]
	v_mfma_i32_16x16x64_i8 v[58:61], v[42:45], v[206:209], v[58:61]
	v_mfma_i32_16x16x64_i8 v[38:41], v[26:29], v[214:217], v[38:41]
	v_mfma_i32_16x16x64_i8 v[34:37], v[42:45], v[214:217], v[34:37]
	v_mfma_i32_16x16x64_i8 v[14:17], v[26:29], v[222:225], v[14:17]
	v_mfma_i32_16x16x64_i8 v[10:13], v[42:45], v[222:225], v[10:13]
	v_mfma_i32_16x16x64_i8 v[78:81], v[30:33], v[202:205], v[78:81]
	v_mfma_i32_16x16x64_i8 v[74:77], v[46:49], v[202:205], v[74:77]
	v_mfma_i32_16x16x64_i8 v[62:65], v[30:33], v[210:213], v[62:65]
	v_mfma_i32_16x16x64_i8 v[58:61], v[46:49], v[210:213], v[58:61]
	v_mfma_i32_16x16x64_i8 v[38:41], v[30:33], v[218:221], v[38:41]
	v_mfma_i32_16x16x64_i8 v[34:37], v[46:49], v[218:221], v[34:37]
	v_mfma_i32_16x16x64_i8 v[14:17], v[30:33], v[226:229], v[14:17]
	v_mfma_i32_16x16x64_i8 v[10:13], v[46:49], v[226:229], v[10:13]
	s_setprio 0
	s_setprio 1
	v_mfma_i32_16x16x64_i8 v[22:25], v[168:171], v[214:217], v[22:25]
	v_mfma_i32_16x16x64_i8 v[18:21], v[176:179], v[214:217], v[18:21]
	v_mfma_i32_16x16x64_i8 v[6:9], v[168:171], v[222:225], v[6:9]
	v_mfma_i32_16x16x64_i8 v[2:5], v[176:179], v[222:225], v[2:5]
	v_mfma_i32_16x16x64_i8 v[26:29], v[168:171], v[198:201], v[70:73]
	v_mfma_i32_16x16x64_i8 v[30:33], v[176:179], v[198:201], v[66:69]
	v_mfma_i32_16x16x64_i8 v[42:45], v[168:171], v[206:209], v[54:57]
	v_mfma_i32_16x16x64_i8 v[46:49], v[176:179], v[206:209], v[50:53]
	v_mfma_i32_16x16x64_i8 v[22:25], v[172:175], v[218:221], v[22:25]
	v_mfma_i32_16x16x64_i8 v[18:21], v[194:197], v[218:221], v[18:21]
	v_mfma_i32_16x16x64_i8 v[6:9], v[172:175], v[226:229], v[6:9]
	v_mfma_i32_16x16x64_i8 v[2:5], v[194:197], v[226:229], v[2:5]
	v_mfma_i32_16x16x64_i8 v[26:29], v[172:175], v[202:205], v[26:29]
	v_mfma_i32_16x16x64_i8 v[30:33], v[194:197], v[202:205], v[30:33]
	v_mfma_i32_16x16x64_i8 v[42:45], v[172:175], v[210:213], v[42:45]
	v_mfma_i32_16x16x64_i8 v[46:49], v[194:197], v[210:213], v[46:49]
	s_setprio 0
	s_add_i32 s38, 0, 0x18000
	s_add_i32 s39, 0, 0x1c000
	s_add_u32 s44, s44, 0x80000
	s_addc_u32 s45, s45, 0
	s_mov_b32 m0, s52
	s_barrier
	v_add_u32_e32 v70, s38, v188
	v_add_u32_e32 v154, s39, v188
	ds_read_b128 v[50:53], v70
	ds_read_b128 v[54:57], v70 offset:1024
	ds_read_b128 v[66:69], v70 offset:2048
	ds_read_b128 v[70:73], v70 offset:3072
	ds_read_b128 v[168:171], v154
	ds_read_b128 v[172:175], v154 offset:1024
	ds_read_b128 v[176:179], v154 offset:2048
	ds_read_b128 v[194:197], v154 offset:3072
	ds_read_b128 v[198:201], v193 offset:32768
	ds_read_b128 v[202:205], v193 offset:33792
	ds_read_b128 v[206:209], v193 offset:34816
	ds_read_b128 v[210:213], v193 offset:35840
	ds_read_b128 v[214:217], v193 offset:36864
	ds_read_b128 v[218:221], v193 offset:37888
	ds_read_b128 v[222:225], v193 offset:38912
	ds_read_b128 v[226:229], v193 offset:39936
	global_load_lds_dwordx4 v146, s[44:45]
	s_mov_b32 m0, s53
	s_nop 0
	global_load_lds_dwordx4 v150, s[44:45]
	s_waitcnt vmcnt(8)
	s_waitcnt lgkmcnt(0)
	s_barrier
	s_setprio 1
	s_waitcnt lgkmcnt(0)
	v_mfma_i32_16x16x64_i8 v[142:145], v[50:53], v[198:201], v[142:145]
	v_mfma_i32_16x16x64_i8 v[138:141], v[66:69], v[198:201], v[138:141]
	v_mfma_i32_16x16x64_i8 v[126:129], v[50:53], v[206:209], v[126:129]
	v_mfma_i32_16x16x64_i8 v[122:125], v[66:69], v[206:209], v[122:125]
	v_mfma_i32_16x16x64_i8 v[110:113], v[50:53], v[214:217], v[110:113]
	v_mfma_i32_16x16x64_i8 v[106:109], v[66:69], v[214:217], v[106:109]
	v_mfma_i32_16x16x64_i8 v[94:97], v[50:53], v[222:225], v[94:97]
	v_mfma_i32_16x16x64_i8 v[90:93], v[66:69], v[222:225], v[90:93]
	v_mfma_i32_16x16x64_i8 v[142:145], v[54:57], v[202:205], v[142:145]
	v_mfma_i32_16x16x64_i8 v[138:141], v[70:73], v[202:205], v[138:141]
	v_mfma_i32_16x16x64_i8 v[126:129], v[54:57], v[210:213], v[126:129]
	v_mfma_i32_16x16x64_i8 v[122:125], v[70:73], v[210:213], v[122:125]
	v_mfma_i32_16x16x64_i8 v[110:113], v[54:57], v[218:221], v[110:113]
	v_mfma_i32_16x16x64_i8 v[106:109], v[70:73], v[218:221], v[106:109]
	v_mfma_i32_16x16x64_i8 v[94:97], v[54:57], v[226:229], v[94:97]
	v_mfma_i32_16x16x64_i8 v[90:93], v[70:73], v[226:229], v[90:93]
	s_setprio 0
	s_setprio 1
	v_mfma_i32_16x16x64_i8 v[134:137], v[168:171], v[198:201], v[134:137]
	v_mfma_i32_16x16x64_i8 v[130:133], v[176:179], v[198:201], v[130:133]
	v_mfma_i32_16x16x64_i8 v[118:121], v[168:171], v[206:209], v[118:121]
	v_mfma_i32_16x16x64_i8 v[114:117], v[176:179], v[206:209], v[114:117]
	v_mfma_i32_16x16x64_i8 v[102:105], v[168:171], v[214:217], v[102:105]
	v_mfma_i32_16x16x64_i8 v[98:101], v[176:179], v[214:217], v[98:101]
	v_mfma_i32_16x16x64_i8 v[86:89], v[168:171], v[222:225], v[86:89]
	v_mfma_i32_16x16x64_i8 v[82:85], v[176:179], v[222:225], v[82:85]
	v_mfma_i32_16x16x64_i8 v[134:137], v[172:175], v[202:205], v[134:137]
	v_mfma_i32_16x16x64_i8 v[130:133], v[194:197], v[202:205], v[130:133]
	v_mfma_i32_16x16x64_i8 v[118:121], v[172:175], v[210:213], v[118:121]
	v_mfma_i32_16x16x64_i8 v[114:117], v[194:197], v[210:213], v[114:117]
	v_mfma_i32_16x16x64_i8 v[102:105], v[172:175], v[218:221], v[102:105]
	v_mfma_i32_16x16x64_i8 v[98:101], v[194:197], v[218:221], v[98:101]
	v_mfma_i32_16x16x64_i8 v[86:89], v[172:175], v[226:229], v[86:89]
	v_mfma_i32_16x16x64_i8 v[82:85], v[194:197], v[226:229], v[82:85]
	s_setprio 0
	s_add_i32 s38, s38, s47
	s_mov_b32 m0, s38
	s_barrier
	ds_read_b128 v[198:201], v193 offset:49152
	ds_read_b128 v[202:205], v193 offset:50176
	ds_read_b128 v[206:209], v193 offset:51200
	ds_read_b128 v[210:213], v193 offset:52224
	ds_read_b128 v[214:217], v193 offset:53248
	ds_read_b128 v[218:221], v193 offset:54272
	ds_read_b128 v[222:225], v193 offset:55296
	ds_read_b128 v[226:229], v193 offset:56320
	global_load_lds_dwordx4 v148, s[98:99]
	s_add_i32 m0, s38, 0x2000
	s_add_u32 s42, s42, 0x80080
	s_addc_u32 s43, s43, 0
	s_add_i32 s38, s39, s47
	global_load_lds_dwordx4 v152, s[98:99]
	s_mov_b32 m0, s38
	s_nop 0
	global_load_lds_dwordx4 v148, s[42:43]
	s_add_i32 m0, s38, 0x2000
	s_nop 0
	global_load_lds_dwordx4 v152, s[42:43]
	s_mov_b32 m0, s58
	s_nop 0
	global_load_lds_dwordx4 v146, s[100:101]
	s_mov_b32 m0, s59
	s_nop 0
	global_load_lds_dwordx4 v150, s[100:101]
	s_waitcnt vmcnt(8)
	s_waitcnt lgkmcnt(0)
	s_barrier
	s_setprio 1
	s_waitcnt lgkmcnt(0)
	v_mfma_i32_16x16x64_i8 v[78:81], v[50:53], v[198:201], v[78:81]
	v_mfma_i32_16x16x64_i8 v[74:77], v[66:69], v[198:201], v[74:77]
	v_mfma_i32_16x16x64_i8 v[62:65], v[50:53], v[206:209], v[62:65]
	v_mfma_i32_16x16x64_i8 v[58:61], v[66:69], v[206:209], v[58:61]
	v_mfma_i32_16x16x64_i8 v[38:41], v[50:53], v[214:217], v[38:41]
	v_mfma_i32_16x16x64_i8 v[34:37], v[66:69], v[214:217], v[34:37]
	v_mfma_i32_16x16x64_i8 v[14:17], v[50:53], v[222:225], v[14:17]
	v_mfma_i32_16x16x64_i8 v[10:13], v[66:69], v[222:225], v[10:13]
	v_mfma_i32_16x16x64_i8 v[78:81], v[54:57], v[202:205], v[78:81]
	v_mfma_i32_16x16x64_i8 v[74:77], v[70:73], v[202:205], v[74:77]
	v_mfma_i32_16x16x64_i8 v[62:65], v[54:57], v[210:213], v[62:65]
	v_mfma_i32_16x16x64_i8 v[58:61], v[70:73], v[210:213], v[58:61]
	v_mfma_i32_16x16x64_i8 v[38:41], v[54:57], v[218:221], v[38:41]
	v_mfma_i32_16x16x64_i8 v[34:37], v[70:73], v[218:221], v[34:37]
	v_mfma_i32_16x16x64_i8 v[14:17], v[54:57], v[226:229], v[14:17]
	v_mfma_i32_16x16x64_i8 v[10:13], v[70:73], v[226:229], v[10:13]
	s_setprio 0
	s_setprio 1
	v_mfma_i32_16x16x64_i8 v[26:29], v[168:171], v[198:201], v[26:29]
	v_mfma_i32_16x16x64_i8 v[70:73], v[172:175], v[202:205], v[26:29]
	v_mfma_i32_16x16x64_i8 v[26:29], v[176:179], v[198:201], v[30:33]
	v_mfma_i32_16x16x64_i8 v[66:69], v[194:197], v[202:205], v[26:29]
	v_mfma_i32_16x16x64_i8 v[26:29], v[168:171], v[206:209], v[42:45]
	v_mfma_i32_16x16x64_i8 v[54:57], v[172:175], v[210:213], v[26:29]
	v_mfma_i32_16x16x64_i8 v[26:29], v[176:179], v[206:209], v[46:49]
	v_mfma_i32_16x16x64_i8 v[22:25], v[168:171], v[214:217], v[22:25]
	v_mfma_i32_16x16x64_i8 v[18:21], v[176:179], v[214:217], v[18:21]
	v_mfma_i32_16x16x64_i8 v[6:9], v[168:171], v[222:225], v[6:9]
	v_mfma_i32_16x16x64_i8 v[2:5], v[176:179], v[222:225], v[2:5]
	v_mfma_i32_16x16x64_i8 v[50:53], v[194:197], v[210:213], v[26:29]
	v_mfma_i32_16x16x64_i8 v[22:25], v[172:175], v[218:221], v[22:25]
	v_mfma_i32_16x16x64_i8 v[18:21], v[194:197], v[218:221], v[18:21]
	v_mfma_i32_16x16x64_i8 v[6:9], v[172:175], v[226:229], v[6:9]
	v_mfma_i32_16x16x64_i8 v[2:5], v[194:197], v[226:229], v[2:5]
	s_setprio 0
	s_add_i32 s74, s74, 2
	s_add_u32 s34, s34, 0x100
	s_addc_u32 s35, s35, 0
	s_add_u32 s67, s67, 0x100
	s_addc_u32 s73, s73, 0
	s_cmp_gt_u32 s74, 29
	s_cbranch_scc1 .Lrot_P2b_exit
	s_add_u32 s38, s34, 0xfff80080
	s_addc_u32 s39, s35, -1
	s_cmp_eq_u32 s74, 28
	s_cselect_b32 s45, s5, s39
	s_cselect_b32 s44, s7, s38
	s_cselect_b32 s43, s8, s73
	s_cselect_b32 s42, s65, s67
	s_add_i32 m0, s50, 0xc000
	s_branch .Lrot_P2b_head
.Lrot_P2b_exit:
	s_barrier
	s_and_b64 vcc, exec, s[14:15]
	s_cbranch_vccz .LBB0_550
	s_barrier

.LBB0_672:
	s_ashr_i32 s25, s24, 31
	s_lshl_b64 s[36:37], s[24:25], 20
	s_add_u32 s36, s50, s36
	s_addc_u32 s37, s51, s37
	s_and_b64 s[46:47], s[2:3], exec
	s_cselect_b32 s25, s37, s45
	s_cselect_b32 s73, s36, s44
	s_ashr_i32 s15, s14, 31
	s_lshl_b64 s[46:47], s[14:15], 20
	s_add_u32 s64, s96, s46
	s_addc_u32 s65, s97, s47
	s_and_b64 s[46:47], s[2:3], exec
	s_cselect_b32 s15, s65, s43
	s_cselect_b32 s74, s64, s42
	s_add_u32 s44, s44, 0x80080
	s_addc_u32 s45, s45, 0
	s_add_u32 s75, s42, 0x100
	v_mov_b32_e32 v2, 0
	s_addc_u32 s76, s43, 0
	s_mov_b32 s77, -2
	v_mov_b32_e32 v3, v2
	v_mov_b32_e32 v4, v2
	v_mov_b32_e32 v5, v2
	v_mov_b32_e32 v6, v2
	v_mov_b32_e32 v7, v2
	v_mov_b32_e32 v8, v2
	v_mov_b32_e32 v9, v2
	v_mov_b32_e32 v18, v2
	v_mov_b32_e32 v19, v2
	v_mov_b32_e32 v20, v2
	v_mov_b32_e32 v21, v2
	v_mov_b32_e32 v22, v2
	v_mov_b32_e32 v23, v2
	v_mov_b32_e32 v24, v2
	v_mov_b32_e32 v25, v2
	v_mov_b32_e32 v34, v2
	v_mov_b32_e32 v35, v2
	v_mov_b32_e32 v36, v2
	v_mov_b32_e32 v37, v2
	v_mov_b32_e32 v38, v2
	v_mov_b32_e32 v39, v2
	v_mov_b32_e32 v40, v2
	v_mov_b32_e32 v41, v2
	v_mov_b32_e32 v50, v2
	v_mov_b32_e32 v51, v2
	v_mov_b32_e32 v52, v2
	v_mov_b32_e32 v53, v2
	v_mov_b32_e32 v54, v2
	v_mov_b32_e32 v55, v2
	v_mov_b32_e32 v56, v2
	v_mov_b32_e32 v57, v2
	v_mov_b32_e32 v10, v2
	v_mov_b32_e32 v11, v2
	v_mov_b32_e32 v12, v2
	v_mov_b32_e32 v13, v2
	v_mov_b32_e32 v14, v2
	v_mov_b32_e32 v15, v2
	v_mov_b32_e32 v16, v2
	v_mov_b32_e32 v17, v2
	v_mov_b32_e32 v26, v2
	v_mov_b32_e32 v27, v2
	v_mov_b32_e32 v28, v2
	v_mov_b32_e32 v29, v2
	v_mov_b32_e32 v30, v2
	v_mov_b32_e32 v31, v2
	v_mov_b32_e32 v32, v2
	v_mov_b32_e32 v33, v2
	v_mov_b32_e32 v42, v2
	v_mov_b32_e32 v43, v2
	v_mov_b32_e32 v44, v2
	v_mov_b32_e32 v45, v2
	v_mov_b32_e32 v46, v2
	v_mov_b32_e32 v47, v2
	v_mov_b32_e32 v48, v2
	v_mov_b32_e32 v49, v2
	v_mov_b32_e32 v58, v2
	v_mov_b32_e32 v59, v2
	v_mov_b32_e32 v60, v2
	v_mov_b32_e32 v61, v2
	v_mov_b32_e32 v62, v2
	v_mov_b32_e32 v63, v2
	v_mov_b32_e32 v64, v2
	v_mov_b32_e32 v65, v2
	v_mov_b32_e32 v66, v2
	v_mov_b32_e32 v67, v2
	v_mov_b32_e32 v68, v2
	v_mov_b32_e32 v69, v2
	v_mov_b32_e32 v70, v2
	v_mov_b32_e32 v71, v2
	v_mov_b32_e32 v72, v2
	v_mov_b32_e32 v73, v2
	v_mov_b32_e32 v82, v2
	v_mov_b32_e32 v83, v2
	v_mov_b32_e32 v84, v2
	v_mov_b32_e32 v85, v2
	v_mov_b32_e32 v86, v2
	v_mov_b32_e32 v87, v2
	v_mov_b32_e32 v88, v2
	v_mov_b32_e32 v89, v2
	v_mov_b32_e32 v98, v2
	v_mov_b32_e32 v99, v2
	v_mov_b32_e32 v100, v2
	v_mov_b32_e32 v101, v2
	v_mov_b32_e32 v102, v2
	v_mov_b32_e32 v103, v2
	v_mov_b32_e32 v104, v2
	v_mov_b32_e32 v105, v2
	v_mov_b32_e32 v114, v2
	v_mov_b32_e32 v115, v2
	v_mov_b32_e32 v116, v2
	v_mov_b32_e32 v117, v2
	v_mov_b32_e32 v118, v2
	v_mov_b32_e32 v119, v2
	v_mov_b32_e32 v120, v2
	v_mov_b32_e32 v121, v2
	v_mov_b32_e32 v74, v2
	v_mov_b32_e32 v75, v2
	v_mov_b32_e32 v76, v2
	v_mov_b32_e32 v77, v2
	v_mov_b32_e32 v78, v2
	v_mov_b32_e32 v79, v2
	v_mov_b32_e32 v80, v2
	v_mov_b32_e32 v81, v2
	v_mov_b32_e32 v90, v2
	v_mov_b32_e32 v91, v2
	v_mov_b32_e32 v92, v2
	v_mov_b32_e32 v93, v2
	v_mov_b32_e32 v94, v2
	v_mov_b32_e32 v95, v2
	v_mov_b32_e32 v96, v2
	v_mov_b32_e32 v97, v2
	v_mov_b32_e32 v106, v2
	v_mov_b32_e32 v107, v2
	v_mov_b32_e32 v108, v2
	v_mov_b32_e32 v109, v2
	v_mov_b32_e32 v110, v2
	v_mov_b32_e32 v111, v2
	v_mov_b32_e32 v112, v2
	v_mov_b32_e32 v113, v2
	v_mov_b32_e32 v138, v2
	v_mov_b32_e32 v139, v2
	v_mov_b32_e32 v140, v2
	v_mov_b32_e32 v141, v2
	v_mov_b32_e32 v142, v2
	v_mov_b32_e32 v143, v2
	v_mov_b32_e32 v144, v2
	v_mov_b32_e32 v145, v2
	s_add_u32 s38, s44, 0xfff80080
	s_addc_u32 s39, s45, -1
	s_cmp_eq_u32 s77, 28
	s_cselect_b32 s47, s25, s39
	s_cselect_b32 s46, s73, s38
	s_cselect_b32 s43, s15, s76
	s_cselect_b32 s42, s74, s75
	s_add_i32 m0, s35, 0xc000
	s_branch .Lrot_P2c_body

.Lrot_P2c_body:
.LBB0_673:
	ds_read_b128 v[122:125], v167
	ds_read_b128 v[126:129], v167 offset:1024
	ds_read_b128 v[130:133], v167 offset:2048
	ds_read_b128 v[134:137], v167 offset:3072
	ds_read_b128 v[174:177], v171
	ds_read_b128 v[178:181], v171 offset:1024
	ds_read_b128 v[182:185], v171 offset:2048
	ds_read_b128 v[186:189], v171 offset:3072
	ds_read_b128 v[190:193], v172
	ds_read_b128 v[194:197], v172 offset:1024
	ds_read_b128 v[198:201], v172 offset:2048
	ds_read_b128 v[202:205], v172 offset:3072
	ds_read_b128 v[206:209], v172 offset:4096
	ds_read_b128 v[210:213], v172 offset:5120
	ds_read_b128 v[214:217], v172 offset:6144
	ds_read_b128 v[218:221], v172 offset:7168
	global_load_lds_dwordx4 v156, s[44:45]
	s_add_i32 m0, s35, 0xe000
	s_nop 0
	global_load_lds_dwordx4 v158, s[44:45]
	s_waitcnt vmcnt(8)
	s_waitcnt lgkmcnt(0)
	s_barrier
	s_setprio 1
	s_waitcnt lgkmcnt(0)
	v_mfma_i32_16x16x64_i8 v[142:145], v[122:125], v[190:193], v[142:145]
	v_mfma_i32_16x16x64_i8 v[138:141], v[130:133], v[190:193], v[138:141]
	v_mfma_i32_16x16x64_i8 v[110:113], v[122:125], v[198:201], v[110:113]
	v_mfma_i32_16x16x64_i8 v[106:109], v[130:133], v[198:201], v[106:109]
	v_mfma_i32_16x16x64_i8 v[94:97], v[122:125], v[206:209], v[94:97]
	v_mfma_i32_16x16x64_i8 v[90:93], v[130:133], v[206:209], v[90:93]
	v_mfma_i32_16x16x64_i8 v[78:81], v[122:125], v[214:217], v[78:81]
	v_mfma_i32_16x16x64_i8 v[74:77], v[130:133], v[214:217], v[74:77]
	v_mfma_i32_16x16x64_i8 v[142:145], v[126:129], v[194:197], v[142:145]
	v_mfma_i32_16x16x64_i8 v[138:141], v[134:137], v[194:197], v[138:141]
	v_mfma_i32_16x16x64_i8 v[110:113], v[126:129], v[202:205], v[110:113]
	v_mfma_i32_16x16x64_i8 v[106:109], v[134:137], v[202:205], v[106:109]
	v_mfma_i32_16x16x64_i8 v[94:97], v[126:129], v[210:213], v[94:97]
	v_mfma_i32_16x16x64_i8 v[90:93], v[134:137], v[210:213], v[90:93]
	v_mfma_i32_16x16x64_i8 v[78:81], v[126:129], v[218:221], v[78:81]
	v_mfma_i32_16x16x64_i8 v[74:77], v[134:137], v[218:221], v[74:77]
	s_setprio 0
	s_setprio 1
	v_mfma_i32_16x16x64_i8 v[118:121], v[174:177], v[190:193], v[118:121]
	v_mfma_i32_16x16x64_i8 v[114:117], v[182:185], v[190:193], v[114:117]
	v_mfma_i32_16x16x64_i8 v[102:105], v[174:177], v[198:201], v[102:105]
	v_mfma_i32_16x16x64_i8 v[98:101], v[182:185], v[198:201], v[98:101]
	v_mfma_i32_16x16x64_i8 v[86:89], v[174:177], v[206:209], v[86:89]
	v_mfma_i32_16x16x64_i8 v[82:85], v[182:185], v[206:209], v[82:85]
	v_mfma_i32_16x16x64_i8 v[70:73], v[174:177], v[214:217], v[70:73]
	v_mfma_i32_16x16x64_i8 v[66:69], v[182:185], v[214:217], v[66:69]
	v_mfma_i32_16x16x64_i8 v[118:121], v[178:181], v[194:197], v[118:121]
	v_mfma_i32_16x16x64_i8 v[114:117], v[186:189], v[194:197], v[114:117]
	v_mfma_i32_16x16x64_i8 v[102:105], v[178:181], v[202:205], v[102:105]
	v_mfma_i32_16x16x64_i8 v[98:101], v[186:189], v[202:205], v[98:101]
	v_mfma_i32_16x16x64_i8 v[86:89], v[178:181], v[210:213], v[86:89]
	v_mfma_i32_16x16x64_i8 v[82:85], v[186:189], v[210:213], v[82:85]
	v_mfma_i32_16x16x64_i8 v[70:73], v[178:181], v[218:221], v[70:73]
	v_mfma_i32_16x16x64_i8 v[66:69], v[186:189], v[218:221], v[66:69]
	s_setprio 0
	s_add_u32 s98, s42, s6
	s_addc_u32 s99, s43, s7
	s_add_u32 s100, s46, s6
	s_addc_u32 s101, s47, s7
	s_add_i32 s38, s66, s52
	s_mov_b32 m0, s38
	s_barrier
	ds_read_b128 v[190:193], v172 offset:16384
	ds_read_b128 v[194:197], v172 offset:17408
	ds_read_b128 v[198:201], v172 offset:18432
	ds_read_b128 v[202:205], v172 offset:19456
	ds_read_b128 v[206:209], v172 offset:20480
	ds_read_b128 v[210:213], v172 offset:21504
	ds_read_b128 v[214:217], v172 offset:22528
	ds_read_b128 v[218:221], v172 offset:23552
	global_load_lds_dwordx4 v148, s[42:43]
	s_add_i32 m0, s38, 0x2000
	s_add_u32 s78, s42, 0x80000
	s_addc_u32 s79, s43, 0
	s_add_i32 s38, s67, s52
	global_load_lds_dwordx4 v152, s[42:43]
	s_mov_b32 m0, s38
	s_nop 0
	global_load_lds_dwordx4 v148, s[78:79]
	s_add_i32 m0, s38, 0x2000
	s_nop 0
	global_load_lds_dwordx4 v152, s[78:79]
	s_mov_b32 m0, s35
	s_nop 0
	global_load_lds_dwordx4 v146, s[46:47]
	s_mov_b32 m0, s53
	s_nop 0
	global_load_lds_dwordx4 v150, s[46:47]
	s_waitcnt vmcnt(8)
	s_waitcnt lgkmcnt(0)
	s_barrier
	s_setprio 1
	s_waitcnt lgkmcnt(0)
	v_mfma_i32_16x16x64_i8 v[62:65], v[122:125], v[190:193], v[62:65]
	v_mfma_i32_16x16x64_i8 v[58:61], v[130:133], v[190:193], v[58:61]
	v_mfma_i32_16x16x64_i8 v[46:49], v[122:125], v[198:201], v[46:49]
	v_mfma_i32_16x16x64_i8 v[42:45], v[130:133], v[198:201], v[42:45]
	v_mfma_i32_16x16x64_i8 v[30:33], v[122:125], v[206:209], v[30:33]
	v_mfma_i32_16x16x64_i8 v[26:29], v[130:133], v[206:209], v[26:29]
	v_mfma_i32_16x16x64_i8 v[14:17], v[122:125], v[214:217], v[14:17]
	v_mfma_i32_16x16x64_i8 v[10:13], v[130:133], v[214:217], v[10:13]
	v_mfma_i32_16x16x64_i8 v[62:65], v[126:129], v[194:197], v[62:65]
	v_mfma_i32_16x16x64_i8 v[58:61], v[134:137], v[194:197], v[58:61]
	v_mfma_i32_16x16x64_i8 v[46:49], v[126:129], v[202:205], v[46:49]
	v_mfma_i32_16x16x64_i8 v[42:45], v[134:137], v[202:205], v[42:45]
	v_mfma_i32_16x16x64_i8 v[30:33], v[126:129], v[210:213], v[30:33]
	v_mfma_i32_16x16x64_i8 v[26:29], v[134:137], v[210:213], v[26:29]
	v_mfma_i32_16x16x64_i8 v[14:17], v[126:129], v[218:221], v[14:17]
	v_mfma_i32_16x16x64_i8 v[10:13], v[134:137], v[218:221], v[10:13]
	s_setprio 0
	s_setprio 1
	v_mfma_i32_16x16x64_i8 v[54:57], v[174:177], v[190:193], v[54:57]
	v_mfma_i32_16x16x64_i8 v[50:53], v[182:185], v[190:193], v[50:53]
	v_mfma_i32_16x16x64_i8 v[38:41], v[174:177], v[198:201], v[38:41]
	v_mfma_i32_16x16x64_i8 v[34:37], v[182:185], v[198:201], v[34:37]
	v_mfma_i32_16x16x64_i8 v[22:25], v[174:177], v[206:209], v[22:25]
	v_mfma_i32_16x16x64_i8 v[18:21], v[182:185], v[206:209], v[18:21]
	v_mfma_i32_16x16x64_i8 v[6:9], v[174:177], v[214:217], v[6:9]
	v_mfma_i32_16x16x64_i8 v[2:5], v[182:185], v[214:217], v[2:5]
	v_mfma_i32_16x16x64_i8 v[54:57], v[178:181], v[194:197], v[54:57]
	v_mfma_i32_16x16x64_i8 v[50:53], v[186:189], v[194:197], v[50:53]
	v_mfma_i32_16x16x64_i8 v[38:41], v[178:181], v[202:205], v[38:41]
	v_mfma_i32_16x16x64_i8 v[34:37], v[186:189], v[202:205], v[34:37]
	v_mfma_i32_16x16x64_i8 v[22:25], v[178:181], v[210:213], v[22:25]
	v_mfma_i32_16x16x64_i8 v[18:21], v[186:189], v[210:213], v[18:21]
	v_mfma_i32_16x16x64_i8 v[6:9], v[178:181], v[218:221], v[6:9]
	v_mfma_i32_16x16x64_i8 v[2:5], v[186:189], v[218:221], v[2:5]
	s_setprio 0
	s_add_i32 s38, 0, 0x18000
	s_add_i32 s39, 0, 0x1c000
	s_add_u32 s46, s46, 0x80000
	s_addc_u32 s47, s47, 0
	s_mov_b32 m0, s58
	s_barrier
	v_add_u32_e32 v134, s38, v169
	v_add_u32_e32 v154, s39, v169
	ds_read_b128 v[122:125], v134
	ds_read_b128 v[126:129], v134 offset:1024
	ds_read_b128 v[130:133], v134 offset:2048
	ds_read_b128 v[134:137], v134 offset:3072
	ds_read_b128 v[174:177], v154
	ds_read_b128 v[178:181], v154 offset:1024
	ds_read_b128 v[182:185], v154 offset:2048
	ds_read_b128 v[186:189], v154 offset:3072
	ds_read_b128 v[190:193], v172 offset:32768
	ds_read_b128 v[194:197], v172 offset:33792
	ds_read_b128 v[198:201], v172 offset:34816
	ds_read_b128 v[202:205], v172 offset:35840
	ds_read_b128 v[206:209], v172 offset:36864
	ds_read_b128 v[210:213], v172 offset:37888
	ds_read_b128 v[214:217], v172 offset:38912
	ds_read_b128 v[218:221], v172 offset:39936
	global_load_lds_dwordx4 v146, s[46:47]
	s_mov_b32 m0, s59
	s_nop 0
	global_load_lds_dwordx4 v150, s[46:47]
	s_waitcnt vmcnt(8)
	s_waitcnt lgkmcnt(0)
	s_barrier
	s_setprio 1
	s_waitcnt lgkmcnt(0)
	v_mfma_i32_16x16x64_i8 v[142:145], v[122:125], v[190:193], v[142:145]
	v_mfma_i32_16x16x64_i8 v[138:141], v[130:133], v[190:193], v[138:141]
	v_mfma_i32_16x16x64_i8 v[110:113], v[122:125], v[198:201], v[110:113]
	v_mfma_i32_16x16x64_i8 v[106:109], v[130:133], v[198:201], v[106:109]
	v_mfma_i32_16x16x64_i8 v[94:97], v[122:125], v[206:209], v[94:97]
	v_mfma_i32_16x16x64_i8 v[90:93], v[130:133], v[206:209], v[90:93]
	v_mfma_i32_16x16x64_i8 v[78:81], v[122:125], v[214:217], v[78:81]
	v_mfma_i32_16x16x64_i8 v[74:77], v[130:133], v[214:217], v[74:77]
	v_mfma_i32_16x16x64_i8 v[142:145], v[126:129], v[194:197], v[142:145]
	v_mfma_i32_16x16x64_i8 v[138:141], v[134:137], v[194:197], v[138:141]
	v_mfma_i32_16x16x64_i8 v[110:113], v[126:129], v[202:205], v[110:113]
	v_mfma_i32_16x16x64_i8 v[106:109], v[134:137], v[202:205], v[106:109]
	v_mfma_i32_16x16x64_i8 v[94:97], v[126:129], v[210:213], v[94:97]
	v_mfma_i32_16x16x64_i8 v[90:93], v[134:137], v[210:213], v[90:93]
	v_mfma_i32_16x16x64_i8 v[78:81], v[126:129], v[218:221], v[78:81]
	v_mfma_i32_16x16x64_i8 v[74:77], v[134:137], v[218:221], v[74:77]
	s_setprio 0
	s_setprio 1
	v_mfma_i32_16x16x64_i8 v[118:121], v[174:177], v[190:193], v[118:121]
	v_mfma_i32_16x16x64_i8 v[114:117], v[182:185], v[190:193], v[114:117]
	v_mfma_i32_16x16x64_i8 v[102:105], v[174:177], v[198:201], v[102:105]
	v_mfma_i32_16x16x64_i8 v[98:101], v[182:185], v[198:201], v[98:101]
	v_mfma_i32_16x16x64_i8 v[86:89], v[174:177], v[206:209], v[86:89]
	v_mfma_i32_16x16x64_i8 v[82:85], v[182:185], v[206:209], v[82:85]
	v_mfma_i32_16x16x64_i8 v[70:73], v[174:177], v[214:217], v[70:73]
	v_mfma_i32_16x16x64_i8 v[66:69], v[182:185], v[214:217], v[66:69]
	v_mfma_i32_16x16x64_i8 v[118:121], v[178:181], v[194:197], v[118:121]
	v_mfma_i32_16x16x64_i8 v[114:117], v[186:189], v[194:197], v[114:117]
	v_mfma_i32_16x16x64_i8 v[102:105], v[178:181], v[202:205], v[102:105]
	v_mfma_i32_16x16x64_i8 v[98:101], v[186:189], v[202:205], v[98:101]
	v_mfma_i32_16x16x64_i8 v[86:89], v[178:181], v[210:213], v[86:89]
	v_mfma_i32_16x16x64_i8 v[82:85], v[186:189], v[210:213], v[82:85]
	v_mfma_i32_16x16x64_i8 v[70:73], v[178:181], v[218:221], v[70:73]
	v_mfma_i32_16x16x64_i8 v[66:69], v[186:189], v[218:221], v[66:69]
	s_setprio 0
	s_add_i32 s38, s38, s52
	s_mov_b32 m0, s38
	s_barrier
	ds_read_b128 v[190:193], v172 offset:49152
	ds_read_b128 v[194:197], v172 offset:50176
	ds_read_b128 v[198:201], v172 offset:51200
	ds_read_b128 v[202:205], v172 offset:52224
	ds_read_b128 v[206:209], v172 offset:53248
	ds_read_b128 v[210:213], v172 offset:54272
	ds_read_b128 v[214:217], v172 offset:55296
	ds_read_b128 v[218:221], v172 offset:56320
	global_load_lds_dwordx4 v148, s[98:99]
	s_add_i32 m0, s38, 0x2000
	s_add_u32 s42, s42, 0x80080
	s_addc_u32 s43, s43, 0
	s_add_i32 s38, s39, s52
	global_load_lds_dwordx4 v152, s[98:99]
	s_mov_b32 m0, s38
	s_nop 0
	global_load_lds_dwordx4 v148, s[42:43]
	s_add_i32 m0, s38, 0x2000
	s_nop 0
	global_load_lds_dwordx4 v152, s[42:43]
	s_mov_b32 m0, s61
	s_nop 0
	global_load_lds_dwordx4 v146, s[100:101]
	s_mov_b32 m0, s62
	s_nop 0
	global_load_lds_dwordx4 v150, s[100:101]
	s_waitcnt vmcnt(8)
	s_waitcnt lgkmcnt(0)
	s_barrier
	s_setprio 1
	s_waitcnt lgkmcnt(0)
	v_mfma_i32_16x16x64_i8 v[62:65], v[122:125], v[190:193], v[62:65]
	v_mfma_i32_16x16x64_i8 v[58:61], v[130:133], v[190:193], v[58:61]
	v_mfma_i32_16x16x64_i8 v[46:49], v[122:125], v[198:201], v[46:49]
	v_mfma_i32_16x16x64_i8 v[42:45], v[130:133], v[198:201], v[42:45]
	v_mfma_i32_16x16x64_i8 v[30:33], v[122:125], v[206:209], v[30:33]
	v_mfma_i32_16x16x64_i8 v[26:29], v[130:133], v[206:209], v[26:29]
	v_mfma_i32_16x16x64_i8 v[14:17], v[122:125], v[214:217], v[14:17]
	v_mfma_i32_16x16x64_i8 v[10:13], v[130:133], v[214:217], v[10:13]
	v_mfma_i32_16x16x64_i8 v[62:65], v[126:129], v[194:197], v[62:65]
	v_mfma_i32_16x16x64_i8 v[58:61], v[134:137], v[194:197], v[58:61]
	v_mfma_i32_16x16x64_i8 v[46:49], v[126:129], v[202:205], v[46:49]
	v_mfma_i32_16x16x64_i8 v[42:45], v[134:137], v[202:205], v[42:45]
	v_mfma_i32_16x16x64_i8 v[30:33], v[126:129], v[210:213], v[30:33]
	v_mfma_i32_16x16x64_i8 v[26:29], v[134:137], v[210:213], v[26:29]
	v_mfma_i32_16x16x64_i8 v[14:17], v[126:129], v[218:221], v[14:17]
	v_mfma_i32_16x16x64_i8 v[10:13], v[134:137], v[218:221], v[10:13]
	s_setprio 0
	s_setprio 1
	v_mfma_i32_16x16x64_i8 v[54:57], v[174:177], v[190:193], v[54:57]
	v_mfma_i32_16x16x64_i8 v[50:53], v[182:185], v[190:193], v[50:53]
	v_mfma_i32_16x16x64_i8 v[38:41], v[174:177], v[198:201], v[38:41]
	v_mfma_i32_16x16x64_i8 v[34:37], v[182:185], v[198:201], v[34:37]
	v_mfma_i32_16x16x64_i8 v[22:25], v[174:177], v[206:209], v[22:25]
	v_mfma_i32_16x16x64_i8 v[18:21], v[182:185], v[206:209], v[18:21]
	v_mfma_i32_16x16x64_i8 v[6:9], v[174:177], v[214:217], v[6:9]
	v_mfma_i32_16x16x64_i8 v[2:5], v[182:185], v[214:217], v[2:5]
	v_mfma_i32_16x16x64_i8 v[54:57], v[178:181], v[194:197], v[54:57]
	v_mfma_i32_16x16x64_i8 v[50:53], v[186:189], v[194:197], v[50:53]
	v_mfma_i32_16x16x64_i8 v[38:41], v[178:181], v[202:205], v[38:41]
	v_mfma_i32_16x16x64_i8 v[34:37], v[186:189], v[202:205], v[34:37]
	v_mfma_i32_16x16x64_i8 v[22:25], v[178:181], v[210:213], v[22:25]
	v_mfma_i32_16x16x64_i8 v[18:21], v[186:189], v[210:213], v[18:21]
	v_mfma_i32_16x16x64_i8 v[6:9], v[178:181], v[218:221], v[6:9]
	v_mfma_i32_16x16x64_i8 v[2:5], v[186:189], v[218:221], v[2:5]
	s_setprio 0
	s_add_i32 s77, s77, 2
	s_add_u32 s44, s44, 0x100
	s_addc_u32 s45, s45, 0
	s_add_u32 s75, s75, 0x100
	s_addc_u32 s76, s76, 0
	s_cmp_gt_u32 s77, 29
	s_cbranch_scc1 .Lrot_P2c_exit
	s_add_u32 s38, s44, 0xfff80080
	s_addc_u32 s39, s45, -1
	s_cmp_eq_u32 s77, 28
	s_cselect_b32 s47, s25, s39
	s_cselect_b32 s46, s73, s38
	s_cselect_b32 s43, s15, s76
	s_cselect_b32 s42, s74, s75
	s_add_i32 m0, s35, 0xc000
	s_branch .Lrot_P2c_head
.Lrot_P2c_exit:
	s_barrier
	s_and_b64 vcc, exec, s[8:9]
	s_cbranch_vccz .LBB0_676
	s_barrier

.LBB0_1488:
	s_ashr_i32 s17, s16, 31
	s_lshl_b64 s[18:19], s[16:17], 20
	s_add_u32 s18, s62, s18
	s_addc_u32 s19, s63, s19
	s_and_b64 s[20:21], s[2:3], exec
	s_cselect_b32 s17, s19, s25
	s_cselect_b32 s49, s18, s24
	s_ashr_i32 s15, s14, 31
	s_lshl_b64 s[20:21], s[14:15], 20
	s_add_u32 s20, s31, s20
	s_addc_u32 s21, s33, s21
	s_and_b64 s[28:29], s[2:3], exec
	s_cselect_b32 s15, s21, s27
	s_cselect_b32 s50, s20, s26
	s_add_u32 s24, s24, 0x80080
	s_addc_u32 s25, s25, 0
	s_add_u32 s51, s26, 0x100
	v_mov_b32_e32 v2, 0
	s_addc_u32 s52, s27, 0
	s_mov_b32 s53, -2
	v_mov_b32_e32 v3, v2
	v_mov_b32_e32 v4, v2
	v_mov_b32_e32 v5, v2
	v_mov_b32_e32 v6, v2
	v_mov_b32_e32 v7, v2
	v_mov_b32_e32 v8, v2
	v_mov_b32_e32 v9, v2
	v_mov_b32_e32 v18, v2
	v_mov_b32_e32 v19, v2
	v_mov_b32_e32 v20, v2
	v_mov_b32_e32 v21, v2
	v_mov_b32_e32 v22, v2
	v_mov_b32_e32 v23, v2
	v_mov_b32_e32 v24, v2
	v_mov_b32_e32 v25, v2
	v_mov_b32_e32 v34, v2
	v_mov_b32_e32 v35, v2
	v_mov_b32_e32 v36, v2
	v_mov_b32_e32 v37, v2
	v_mov_b32_e32 v38, v2
	v_mov_b32_e32 v39, v2
	v_mov_b32_e32 v40, v2
	v_mov_b32_e32 v41, v2
	v_mov_b32_e32 v50, v2
	v_mov_b32_e32 v51, v2
	v_mov_b32_e32 v52, v2
	v_mov_b32_e32 v53, v2
	v_mov_b32_e32 v54, v2
	v_mov_b32_e32 v55, v2
	v_mov_b32_e32 v56, v2
	v_mov_b32_e32 v57, v2
	v_mov_b32_e32 v10, v2
	v_mov_b32_e32 v11, v2
	v_mov_b32_e32 v12, v2
	v_mov_b32_e32 v13, v2
	v_mov_b32_e32 v14, v2
	v_mov_b32_e32 v15, v2
	v_mov_b32_e32 v16, v2
	v_mov_b32_e32 v17, v2
	v_mov_b32_e32 v26, v2
	v_mov_b32_e32 v27, v2
	v_mov_b32_e32 v28, v2
	v_mov_b32_e32 v29, v2
	v_mov_b32_e32 v30, v2
	v_mov_b32_e32 v31, v2
	v_mov_b32_e32 v32, v2
	v_mov_b32_e32 v33, v2
	v_mov_b32_e32 v42, v2
	v_mov_b32_e32 v43, v2
	v_mov_b32_e32 v44, v2
	v_mov_b32_e32 v45, v2
	v_mov_b32_e32 v46, v2
	v_mov_b32_e32 v47, v2
	v_mov_b32_e32 v48, v2
	v_mov_b32_e32 v49, v2
	v_mov_b32_e32 v58, v2
	v_mov_b32_e32 v59, v2
	v_mov_b32_e32 v60, v2
	v_mov_b32_e32 v61, v2
	v_mov_b32_e32 v62, v2
	v_mov_b32_e32 v63, v2
	v_mov_b32_e32 v64, v2
	v_mov_b32_e32 v65, v2
	v_mov_b32_e32 v66, v2
	v_mov_b32_e32 v67, v2
	v_mov_b32_e32 v68, v2
	v_mov_b32_e32 v69, v2
	v_mov_b32_e32 v70, v2
	v_mov_b32_e32 v71, v2
	v_mov_b32_e32 v72, v2
	v_mov_b32_e32 v73, v2
	v_mov_b32_e32 v82, v2
	v_mov_b32_e32 v83, v2
	v_mov_b32_e32 v84, v2
	v_mov_b32_e32 v85, v2
	v_mov_b32_e32 v86, v2
	v_mov_b32_e32 v87, v2
	v_mov_b32_e32 v88, v2
	v_mov_b32_e32 v89, v2
	v_mov_b32_e32 v98, v2
	v_mov_b32_e32 v99, v2
	v_mov_b32_e32 v100, v2
	v_mov_b32_e32 v101, v2
	v_mov_b32_e32 v102, v2
	v_mov_b32_e32 v103, v2
	v_mov_b32_e32 v104, v2
	v_mov_b32_e32 v105, v2
	v_mov_b32_e32 v114, v2
	v_mov_b32_e32 v115, v2
	v_mov_b32_e32 v116, v2
	v_mov_b32_e32 v117, v2
	v_mov_b32_e32 v118, v2
	v_mov_b32_e32 v119, v2
	v_mov_b32_e32 v120, v2
	v_mov_b32_e32 v121, v2
	v_mov_b32_e32 v74, v2
	v_mov_b32_e32 v75, v2
	v_mov_b32_e32 v76, v2
	v_mov_b32_e32 v77, v2
	v_mov_b32_e32 v78, v2
	v_mov_b32_e32 v79, v2
	v_mov_b32_e32 v80, v2
	v_mov_b32_e32 v81, v2
	v_mov_b32_e32 v90, v2
	v_mov_b32_e32 v91, v2
	v_mov_b32_e32 v92, v2
	v_mov_b32_e32 v93, v2
	v_mov_b32_e32 v94, v2
	v_mov_b32_e32 v95, v2
	v_mov_b32_e32 v96, v2
	v_mov_b32_e32 v97, v2
	v_mov_b32_e32 v106, v2
	v_mov_b32_e32 v107, v2
	v_mov_b32_e32 v108, v2
	v_mov_b32_e32 v109, v2
	v_mov_b32_e32 v110, v2
	v_mov_b32_e32 v111, v2
	v_mov_b32_e32 v112, v2
	v_mov_b32_e32 v113, v2
	v_mov_b32_e32 v138, v2
	v_mov_b32_e32 v139, v2
	v_mov_b32_e32 v140, v2
	v_mov_b32_e32 v141, v2
	v_mov_b32_e32 v142, v2
	v_mov_b32_e32 v143, v2
	v_mov_b32_e32 v144, v2
	v_mov_b32_e32 v145, v2
	s_add_u32 s26, s24, 0xfff80080
	s_addc_u32 s27, s25, -1
	s_cmp_eq_u32 s53, 28
	s_cselect_b32 s29, s17, s27
	s_cselect_b32 s28, s49, s26
	s_cselect_b32 s27, s15, s52
	s_cselect_b32 s26, s50, s51
	s_add_i32 m0, s23, 0xc000
	s_branch .Lrot_P6_body

.Lrot_P6_body:
.LBB0_1489:
	ds_read_b128 v[122:125], v169
	ds_read_b128 v[126:129], v169 offset:1024
	ds_read_b128 v[130:133], v169 offset:2048
	ds_read_b128 v[134:137], v169 offset:3072
	ds_read_b128 v[172:175], v170
	ds_read_b128 v[176:179], v170 offset:1024
	ds_read_b128 v[180:183], v170 offset:2048
	ds_read_b128 v[184:187], v170 offset:3072
	ds_read_b128 v[188:191], v171
	ds_read_b128 v[192:195], v171 offset:1024
	ds_read_b128 v[196:199], v171 offset:2048
	ds_read_b128 v[200:203], v171 offset:3072
	ds_read_b128 v[204:207], v171 offset:4096
	ds_read_b128 v[208:211], v171 offset:5120
	ds_read_b128 v[212:215], v171 offset:6144
	ds_read_b128 v[216:219], v171 offset:7168
	global_load_lds_dwordx4 v156, s[24:25]
	s_add_i32 m0, s23, 0xe000
	s_nop 0
	global_load_lds_dwordx4 v158, s[24:25]
	s_waitcnt vmcnt(8)
	s_waitcnt lgkmcnt(0)
	s_barrier
	s_setprio 1
	s_waitcnt lgkmcnt(0)
	v_mfma_i32_16x16x64_i8 v[142:145], v[122:125], v[188:191], v[142:145]
	v_mfma_i32_16x16x64_i8 v[138:141], v[130:133], v[188:191], v[138:141]
	v_mfma_i32_16x16x64_i8 v[110:113], v[122:125], v[196:199], v[110:113]
	v_mfma_i32_16x16x64_i8 v[106:109], v[130:133], v[196:199], v[106:109]
	v_mfma_i32_16x16x64_i8 v[94:97], v[122:125], v[204:207], v[94:97]
	v_mfma_i32_16x16x64_i8 v[90:93], v[130:133], v[204:207], v[90:93]
	v_mfma_i32_16x16x64_i8 v[78:81], v[122:125], v[212:215], v[78:81]
	v_mfma_i32_16x16x64_i8 v[74:77], v[130:133], v[212:215], v[74:77]
	v_mfma_i32_16x16x64_i8 v[142:145], v[126:129], v[192:195], v[142:145]
	v_mfma_i32_16x16x64_i8 v[138:141], v[134:137], v[192:195], v[138:141]
	v_mfma_i32_16x16x64_i8 v[110:113], v[126:129], v[200:203], v[110:113]
	v_mfma_i32_16x16x64_i8 v[106:109], v[134:137], v[200:203], v[106:109]
	v_mfma_i32_16x16x64_i8 v[94:97], v[126:129], v[208:211], v[94:97]
	v_mfma_i32_16x16x64_i8 v[90:93], v[134:137], v[208:211], v[90:93]
	v_mfma_i32_16x16x64_i8 v[78:81], v[126:129], v[216:219], v[78:81]
	v_mfma_i32_16x16x64_i8 v[74:77], v[134:137], v[216:219], v[74:77]
	s_setprio 0
	s_setprio 1
	v_mfma_i32_16x16x64_i8 v[118:121], v[172:175], v[188:191], v[118:121]
	v_mfma_i32_16x16x64_i8 v[114:117], v[180:183], v[188:191], v[114:117]
	v_mfma_i32_16x16x64_i8 v[102:105], v[172:175], v[196:199], v[102:105]
	v_mfma_i32_16x16x64_i8 v[98:101], v[180:183], v[196:199], v[98:101]
	v_mfma_i32_16x16x64_i8 v[86:89], v[172:175], v[204:207], v[86:89]
	v_mfma_i32_16x16x64_i8 v[82:85], v[180:183], v[204:207], v[82:85]
	v_mfma_i32_16x16x64_i8 v[70:73], v[172:175], v[212:215], v[70:73]
	v_mfma_i32_16x16x64_i8 v[66:69], v[180:183], v[212:215], v[66:69]
	v_mfma_i32_16x16x64_i8 v[118:121], v[176:179], v[192:195], v[118:121]
	v_mfma_i32_16x16x64_i8 v[114:117], v[184:187], v[192:195], v[114:117]
	v_mfma_i32_16x16x64_i8 v[102:105], v[176:179], v[200:203], v[102:105]
	v_mfma_i32_16x16x64_i8 v[98:101], v[184:187], v[200:203], v[98:101]
	v_mfma_i32_16x16x64_i8 v[86:89], v[176:179], v[208:211], v[86:89]
	v_mfma_i32_16x16x64_i8 v[82:85], v[184:187], v[208:211], v[82:85]
	v_mfma_i32_16x16x64_i8 v[70:73], v[176:179], v[216:219], v[70:73]
	v_mfma_i32_16x16x64_i8 v[66:69], v[184:187], v[216:219], v[66:69]
	s_setprio 0
	s_add_u32 s98, s26, s10
	s_addc_u32 s99, s27, s11
	s_add_u32 s100, s28, s10
	s_addc_u32 s101, s29, s11
	s_add_i32 s38, s46, s34
	s_mov_b32 m0, s38
	s_barrier
	ds_read_b128 v[188:191], v171 offset:16384
	ds_read_b128 v[192:195], v171 offset:17408
	ds_read_b128 v[196:199], v171 offset:18432
	ds_read_b128 v[200:203], v171 offset:19456
	ds_read_b128 v[204:207], v171 offset:20480
	ds_read_b128 v[208:211], v171 offset:21504
	ds_read_b128 v[212:215], v171 offset:22528
	ds_read_b128 v[216:219], v171 offset:23552
	global_load_lds_dwordx4 v148, s[26:27]
	s_add_i32 m0, s38, 0x2000
	s_add_u32 s38, s26, 0x80000
	s_addc_u32 s39, s27, 0
	s_add_i32 s54, s47, s34
	global_load_lds_dwordx4 v152, s[26:27]
	s_mov_b32 m0, s54
	s_nop 0
	global_load_lds_dwordx4 v148, s[38:39]
	s_add_i32 m0, s54, 0x2000
	s_nop 0
	global_load_lds_dwordx4 v152, s[38:39]
	s_mov_b32 m0, s23
	s_nop 0
	global_load_lds_dwordx4 v146, s[28:29]
	s_mov_b32 m0, s35
	s_nop 0
	global_load_lds_dwordx4 v150, s[28:29]
	s_waitcnt vmcnt(8)
	s_waitcnt lgkmcnt(0)
	s_barrier
	s_setprio 1
	s_waitcnt lgkmcnt(0)
	v_mfma_i32_16x16x64_i8 v[62:65], v[122:125], v[188:191], v[62:65]
	v_mfma_i32_16x16x64_i8 v[58:61], v[130:133], v[188:191], v[58:61]
	v_mfma_i32_16x16x64_i8 v[46:49], v[122:125], v[196:199], v[46:49]
	v_mfma_i32_16x16x64_i8 v[42:45], v[130:133], v[196:199], v[42:45]
	v_mfma_i32_16x16x64_i8 v[30:33], v[122:125], v[204:207], v[30:33]
	v_mfma_i32_16x16x64_i8 v[26:29], v[130:133], v[204:207], v[26:29]
	v_mfma_i32_16x16x64_i8 v[14:17], v[122:125], v[212:215], v[14:17]
	v_mfma_i32_16x16x64_i8 v[10:13], v[130:133], v[212:215], v[10:13]
	v_mfma_i32_16x16x64_i8 v[62:65], v[126:129], v[192:195], v[62:65]
	v_mfma_i32_16x16x64_i8 v[58:61], v[134:137], v[192:195], v[58:61]
	v_mfma_i32_16x16x64_i8 v[46:49], v[126:129], v[200:203], v[46:49]
	v_mfma_i32_16x16x64_i8 v[42:45], v[134:137], v[200:203], v[42:45]
	v_mfma_i32_16x16x64_i8 v[30:33], v[126:129], v[208:211], v[30:33]
	v_mfma_i32_16x16x64_i8 v[26:29], v[134:137], v[208:211], v[26:29]
	v_mfma_i32_16x16x64_i8 v[14:17], v[126:129], v[216:219], v[14:17]
	v_mfma_i32_16x16x64_i8 v[10:13], v[134:137], v[216:219], v[10:13]
	s_setprio 0
	s_setprio 1
	v_mfma_i32_16x16x64_i8 v[54:57], v[172:175], v[188:191], v[54:57]
	v_mfma_i32_16x16x64_i8 v[50:53], v[180:183], v[188:191], v[50:53]
	v_mfma_i32_16x16x64_i8 v[38:41], v[172:175], v[196:199], v[38:41]
	v_mfma_i32_16x16x64_i8 v[34:37], v[180:183], v[196:199], v[34:37]
	v_mfma_i32_16x16x64_i8 v[22:25], v[172:175], v[204:207], v[22:25]
	v_mfma_i32_16x16x64_i8 v[18:21], v[180:183], v[204:207], v[18:21]
	v_mfma_i32_16x16x64_i8 v[6:9], v[172:175], v[212:215], v[6:9]
	v_mfma_i32_16x16x64_i8 v[2:5], v[180:183], v[212:215], v[2:5]
	v_mfma_i32_16x16x64_i8 v[54:57], v[176:179], v[192:195], v[54:57]
	v_mfma_i32_16x16x64_i8 v[50:53], v[184:187], v[192:195], v[50:53]
	v_mfma_i32_16x16x64_i8 v[38:41], v[176:179], v[200:203], v[38:41]
	v_mfma_i32_16x16x64_i8 v[34:37], v[184:187], v[200:203], v[34:37]
	v_mfma_i32_16x16x64_i8 v[22:25], v[176:179], v[208:211], v[22:25]
	v_mfma_i32_16x16x64_i8 v[18:21], v[184:187], v[208:211], v[18:21]
	v_mfma_i32_16x16x64_i8 v[6:9], v[176:179], v[216:219], v[6:9]
	v_mfma_i32_16x16x64_i8 v[2:5], v[184:187], v[216:219], v[2:5]
	s_setprio 0
	s_add_i32 s38, 0, 0x18000
	s_add_i32 s39, 0, 0x1c000
	s_add_u32 s28, s28, 0x80000
	s_addc_u32 s29, s29, 0
	s_mov_b32 m0, s36
	s_barrier
	v_add_u32_e32 v134, s38, v167
	v_add_u32_e32 v154, s39, v167
	ds_read_b128 v[122:125], v134
	ds_read_b128 v[126:129], v134 offset:1024
	ds_read_b128 v[130:133], v134 offset:2048
	ds_read_b128 v[134:137], v134 offset:3072
	ds_read_b128 v[172:175], v154
	ds_read_b128 v[176:179], v154 offset:1024
	ds_read_b128 v[180:183], v154 offset:2048
	ds_read_b128 v[184:187], v154 offset:3072
	ds_read_b128 v[188:191], v171 offset:32768
	ds_read_b128 v[192:195], v171 offset:33792
	ds_read_b128 v[196:199], v171 offset:34816
	ds_read_b128 v[200:203], v171 offset:35840
	ds_read_b128 v[204:207], v171 offset:36864
	ds_read_b128 v[208:211], v171 offset:37888
	ds_read_b128 v[212:215], v171 offset:38912
	ds_read_b128 v[216:219], v171 offset:39936
	global_load_lds_dwordx4 v146, s[28:29]
	s_mov_b32 m0, s37
	s_nop 0
	global_load_lds_dwordx4 v150, s[28:29]
	s_waitcnt vmcnt(8)
	s_waitcnt lgkmcnt(0)
	s_barrier
	s_setprio 1
	s_waitcnt lgkmcnt(0)
	v_mfma_i32_16x16x64_i8 v[142:145], v[122:125], v[188:191], v[142:145]
	v_mfma_i32_16x16x64_i8 v[138:141], v[130:133], v[188:191], v[138:141]
	v_mfma_i32_16x16x64_i8 v[110:113], v[122:125], v[196:199], v[110:113]
	v_mfma_i32_16x16x64_i8 v[106:109], v[130:133], v[196:199], v[106:109]
	v_mfma_i32_16x16x64_i8 v[94:97], v[122:125], v[204:207], v[94:97]
	v_mfma_i32_16x16x64_i8 v[90:93], v[130:133], v[204:207], v[90:93]
	v_mfma_i32_16x16x64_i8 v[78:81], v[122:125], v[212:215], v[78:81]
	v_mfma_i32_16x16x64_i8 v[74:77], v[130:133], v[212:215], v[74:77]
	v_mfma_i32_16x16x64_i8 v[142:145], v[126:129], v[192:195], v[142:145]
	v_mfma_i32_16x16x64_i8 v[138:141], v[134:137], v[192:195], v[138:141]
	v_mfma_i32_16x16x64_i8 v[110:113], v[126:129], v[200:203], v[110:113]
	v_mfma_i32_16x16x64_i8 v[106:109], v[134:137], v[200:203], v[106:109]
	v_mfma_i32_16x16x64_i8 v[94:97], v[126:129], v[208:211], v[94:97]
	v_mfma_i32_16x16x64_i8 v[90:93], v[134:137], v[208:211], v[90:93]
	v_mfma_i32_16x16x64_i8 v[78:81], v[126:129], v[216:219], v[78:81]
	v_mfma_i32_16x16x64_i8 v[74:77], v[134:137], v[216:219], v[74:77]
	s_setprio 0
	s_setprio 1
	v_mfma_i32_16x16x64_i8 v[118:121], v[172:175], v[188:191], v[118:121]
	v_mfma_i32_16x16x64_i8 v[114:117], v[180:183], v[188:191], v[114:117]
	v_mfma_i32_16x16x64_i8 v[102:105], v[172:175], v[196:199], v[102:105]
	v_mfma_i32_16x16x64_i8 v[98:101], v[180:183], v[196:199], v[98:101]
	v_mfma_i32_16x16x64_i8 v[86:89], v[172:175], v[204:207], v[86:89]
	v_mfma_i32_16x16x64_i8 v[82:85], v[180:183], v[204:207], v[82:85]
	v_mfma_i32_16x16x64_i8 v[70:73], v[172:175], v[212:215], v[70:73]
	v_mfma_i32_16x16x64_i8 v[66:69], v[180:183], v[212:215], v[66:69]
	v_mfma_i32_16x16x64_i8 v[118:121], v[176:179], v[192:195], v[118:121]
	v_mfma_i32_16x16x64_i8 v[114:117], v[184:187], v[192:195], v[114:117]
	v_mfma_i32_16x16x64_i8 v[102:105], v[176:179], v[200:203], v[102:105]
	v_mfma_i32_16x16x64_i8 v[98:101], v[184:187], v[200:203], v[98:101]
	v_mfma_i32_16x16x64_i8 v[86:89], v[176:179], v[208:211], v[86:89]
	v_mfma_i32_16x16x64_i8 v[82:85], v[184:187], v[208:211], v[82:85]
	v_mfma_i32_16x16x64_i8 v[70:73], v[176:179], v[216:219], v[70:73]
	v_mfma_i32_16x16x64_i8 v[66:69], v[184:187], v[216:219], v[66:69]
	s_setprio 0
	s_add_i32 s28, s38, s34
	s_mov_b32 m0, s28
	s_barrier
	ds_read_b128 v[188:191], v171 offset:49152
	ds_read_b128 v[192:195], v171 offset:50176
	ds_read_b128 v[196:199], v171 offset:51200
	ds_read_b128 v[200:203], v171 offset:52224
	ds_read_b128 v[204:207], v171 offset:53248
	ds_read_b128 v[208:211], v171 offset:54272
	ds_read_b128 v[212:215], v171 offset:55296
	ds_read_b128 v[216:219], v171 offset:56320
	global_load_lds_dwordx4 v148, s[98:99]
	s_add_i32 m0, s28, 0x2000
	s_add_u32 s26, s26, 0x80080
	s_addc_u32 s27, s27, 0
	s_add_i32 s28, s39, s34
	global_load_lds_dwordx4 v152, s[98:99]
	s_mov_b32 m0, s28
	s_nop 0
	global_load_lds_dwordx4 v148, s[26:27]
	s_add_i32 m0, s28, 0x2000
	s_nop 0
	global_load_lds_dwordx4 v152, s[26:27]
	s_mov_b32 m0, s43
	s_nop 0
	global_load_lds_dwordx4 v146, s[100:101]
	s_mov_b32 m0, s44
	s_nop 0
	global_load_lds_dwordx4 v150, s[100:101]
	s_waitcnt vmcnt(8)
	s_waitcnt lgkmcnt(0)
	s_barrier
	s_setprio 1
	s_waitcnt lgkmcnt(0)
	v_mfma_i32_16x16x64_i8 v[62:65], v[122:125], v[188:191], v[62:65]
	v_mfma_i32_16x16x64_i8 v[58:61], v[130:133], v[188:191], v[58:61]
	v_mfma_i32_16x16x64_i8 v[46:49], v[122:125], v[196:199], v[46:49]
	v_mfma_i32_16x16x64_i8 v[42:45], v[130:133], v[196:199], v[42:45]
	v_mfma_i32_16x16x64_i8 v[30:33], v[122:125], v[204:207], v[30:33]
	v_mfma_i32_16x16x64_i8 v[26:29], v[130:133], v[204:207], v[26:29]
	v_mfma_i32_16x16x64_i8 v[14:17], v[122:125], v[212:215], v[14:17]
	v_mfma_i32_16x16x64_i8 v[10:13], v[130:133], v[212:215], v[10:13]
	v_mfma_i32_16x16x64_i8 v[62:65], v[126:129], v[192:195], v[62:65]
	v_mfma_i32_16x16x64_i8 v[58:61], v[134:137], v[192:195], v[58:61]
	v_mfma_i32_16x16x64_i8 v[46:49], v[126:129], v[200:203], v[46:49]
	v_mfma_i32_16x16x64_i8 v[42:45], v[134:137], v[200:203], v[42:45]
	v_mfma_i32_16x16x64_i8 v[30:33], v[126:129], v[208:211], v[30:33]
	v_mfma_i32_16x16x64_i8 v[26:29], v[134:137], v[208:211], v[26:29]
	v_mfma_i32_16x16x64_i8 v[14:17], v[126:129], v[216:219], v[14:17]
	v_mfma_i32_16x16x64_i8 v[10:13], v[134:137], v[216:219], v[10:13]
	s_setprio 0
	s_setprio 1
	v_mfma_i32_16x16x64_i8 v[54:57], v[172:175], v[188:191], v[54:57]
	v_mfma_i32_16x16x64_i8 v[50:53], v[180:183], v[188:191], v[50:53]
	v_mfma_i32_16x16x64_i8 v[38:41], v[172:175], v[196:199], v[38:41]
	v_mfma_i32_16x16x64_i8 v[34:37], v[180:183], v[196:199], v[34:37]
	v_mfma_i32_16x16x64_i8 v[22:25], v[172:175], v[204:207], v[22:25]
	v_mfma_i32_16x16x64_i8 v[18:21], v[180:183], v[204:207], v[18:21]
	v_mfma_i32_16x16x64_i8 v[6:9], v[172:175], v[212:215], v[6:9]
	v_mfma_i32_16x16x64_i8 v[2:5], v[180:183], v[212:215], v[2:5]
	v_mfma_i32_16x16x64_i8 v[54:57], v[176:179], v[192:195], v[54:57]
	v_mfma_i32_16x16x64_i8 v[50:53], v[184:187], v[192:195], v[50:53]
	v_mfma_i32_16x16x64_i8 v[38:41], v[176:179], v[200:203], v[38:41]
	v_mfma_i32_16x16x64_i8 v[34:37], v[184:187], v[200:203], v[34:37]
	v_mfma_i32_16x16x64_i8 v[22:25], v[176:179], v[208:211], v[22:25]
	v_mfma_i32_16x16x64_i8 v[18:21], v[184:187], v[208:211], v[18:21]
	v_mfma_i32_16x16x64_i8 v[6:9], v[176:179], v[216:219], v[6:9]
	v_mfma_i32_16x16x64_i8 v[2:5], v[184:187], v[216:219], v[2:5]
	s_setprio 0
	s_add_i32 s53, s53, 2
	s_add_u32 s24, s24, 0x100
	s_addc_u32 s25, s25, 0
	s_add_u32 s51, s51, 0x100
	s_addc_u32 s52, s52, 0
	s_cmp_gt_u32 s53, 29
	s_cbranch_scc1 .Lrot_P6_exit
	s_add_u32 s26, s24, 0xfff80080
	s_addc_u32 s27, s25, -1
	s_cmp_eq_u32 s53, 28
	s_cselect_b32 s29, s17, s27
	s_cselect_b32 s28, s49, s26
	s_cselect_b32 s27, s15, s52
	s_cselect_b32 s26, s50, s51
	s_add_i32 m0, s23, 0xc000
	s_branch .Lrot_P6_head

.LBB0_1648:
	s_ashr_i32 s29, s28, 31
	s_lshl_b64 s[30:31], s[28:29], 20
	v_readlane_b32 s36, v254, 42
	v_readlane_b32 s37, v254, 43
	s_add_u32 s30, s36, s30
	s_addc_u32 s31, s37, s31
	s_and_b64 s[36:37], s[2:3], exec
	s_cselect_b32 s1, s31, s35
	s_cselect_b32 s29, s30, s34
	s_ashr_i32 s27, s26, 31
	s_lshl_b64 s[36:37], s[26:27], 20
	s_add_u32 s36, s33, s36
	s_addc_u32 s37, s48, s37
	s_and_b64 s[38:39], s[2:3], exec
	s_cselect_b32 s27, s37, s43
	s_cselect_b32 s41, s36, s42
	s_add_u32 s34, s34, 0x80080
	s_addc_u32 s35, s35, 0
	s_add_u32 s46, s42, 0x100
	v_mov_b32_e32 v98, 0
	s_addc_u32 s47, s43, 0
	s_mov_b32 s77, -2
	v_mov_b32_e32 v99, v98
	v_mov_b32_e32 v100, v98
	v_mov_b32_e32 v101, v98
	v_mov_b32_e32 v102, v98
	v_mov_b32_e32 v103, v98
	v_mov_b32_e32 v104, v98
	v_mov_b32_e32 v105, v98
	v_mov_b32_e32 v50, v98
	v_mov_b32_e32 v51, v98
	v_mov_b32_e32 v52, v98
	v_mov_b32_e32 v53, v98
	v_mov_b32_e32 v74, v98
	v_mov_b32_e32 v75, v98
	v_mov_b32_e32 v76, v98
	v_mov_b32_e32 v77, v98
	v_mov_b32_e32 v58, v98
	v_mov_b32_e32 v59, v98
	v_mov_b32_e32 v60, v98
	v_mov_b32_e32 v61, v98
	v_mov_b32_e32 v82, v98
	v_mov_b32_e32 v83, v98
	v_mov_b32_e32 v84, v98
	v_mov_b32_e32 v85, v98
	v_mov_b32_e32 v66, v98
	v_mov_b32_e32 v67, v98
	v_mov_b32_e32 v68, v98
	v_mov_b32_e32 v69, v98
	v_mov_b32_e32 v90, v98
	v_mov_b32_e32 v91, v98
	v_mov_b32_e32 v92, v98
	v_mov_b32_e32 v93, v98
	v_mov_b32_e32 v106, v98
	v_mov_b32_e32 v107, v98
	v_mov_b32_e32 v108, v98
	v_mov_b32_e32 v109, v98
	v_mov_b32_e32 v110, v98
	v_mov_b32_e32 v111, v98
	v_mov_b32_e32 v112, v98
	v_mov_b32_e32 v113, v98
	v_mov_b32_e32 v54, v98
	v_mov_b32_e32 v55, v98
	v_mov_b32_e32 v56, v98
	v_mov_b32_e32 v57, v98
	v_mov_b32_e32 v78, v98
	v_mov_b32_e32 v79, v98
	v_mov_b32_e32 v80, v98
	v_mov_b32_e32 v81, v98
	v_mov_b32_e32 v62, v98
	v_mov_b32_e32 v63, v98
	v_mov_b32_e32 v64, v98
	v_mov_b32_e32 v65, v98
	v_mov_b32_e32 v86, v98
	v_mov_b32_e32 v87, v98
	v_mov_b32_e32 v88, v98
	v_mov_b32_e32 v89, v98
	v_mov_b32_e32 v70, v98
	v_mov_b32_e32 v71, v98
	v_mov_b32_e32 v72, v98
	v_mov_b32_e32 v73, v98
	v_mov_b32_e32 v94, v98
	v_mov_b32_e32 v95, v98
	v_mov_b32_e32 v96, v98
	v_mov_b32_e32 v97, v98
	v_mov_b32_e32 v114, v98
	v_mov_b32_e32 v115, v98
	v_mov_b32_e32 v116, v98
	v_mov_b32_e32 v117, v98
	v_mov_b32_e32 v118, v98
	v_mov_b32_e32 v119, v98
	v_mov_b32_e32 v120, v98
	v_mov_b32_e32 v121, v98
	v_mov_b32_e32 v2, v98
	v_mov_b32_e32 v3, v98
	v_mov_b32_e32 v4, v98
	v_mov_b32_e32 v5, v98
	v_mov_b32_e32 v14, v98
	v_mov_b32_e32 v15, v98
	v_mov_b32_e32 v16, v98
	v_mov_b32_e32 v17, v98
	v_mov_b32_e32 v6, v98
	v_mov_b32_e32 v7, v98
	v_mov_b32_e32 v8, v98
	v_mov_b32_e32 v9, v98
	v_mov_b32_e32 v18, v98
	v_mov_b32_e32 v19, v98
	v_mov_b32_e32 v20, v98
	v_mov_b32_e32 v21, v98
	v_mov_b32_e32 v10, v98
	v_mov_b32_e32 v11, v98
	v_mov_b32_e32 v12, v98
	v_mov_b32_e32 v13, v98
	v_mov_b32_e32 v22, v98
	v_mov_b32_e32 v23, v98
	v_mov_b32_e32 v24, v98
	v_mov_b32_e32 v25, v98
	v_mov_b32_e32 v122, v98
	v_mov_b32_e32 v123, v98
	v_mov_b32_e32 v124, v98
	v_mov_b32_e32 v125, v98
	v_mov_b32_e32 v126, v98
	v_mov_b32_e32 v127, v98
	v_mov_b32_e32 v128, v98
	v_mov_b32_e32 v129, v98
	v_mov_b32_e32 v26, v98
	v_mov_b32_e32 v27, v98
	v_mov_b32_e32 v28, v98
	v_mov_b32_e32 v29, v98
	v_mov_b32_e32 v38, v98
	v_mov_b32_e32 v39, v98
	v_mov_b32_e32 v40, v98
	v_mov_b32_e32 v41, v98
	v_mov_b32_e32 v30, v98
	v_mov_b32_e32 v31, v98
	v_mov_b32_e32 v32, v98
	v_mov_b32_e32 v33, v98
	v_mov_b32_e32 v42, v98
	v_mov_b32_e32 v43, v98
	v_mov_b32_e32 v44, v98
	v_mov_b32_e32 v45, v98
	v_mov_b32_e32 v34, v98
	v_mov_b32_e32 v35, v98
	v_mov_b32_e32 v36, v98
	v_mov_b32_e32 v37, v98
	v_mov_b32_e32 v46, v98
	v_mov_b32_e32 v47, v98
	v_mov_b32_e32 v48, v98
	v_mov_b32_e32 v49, v98
	s_add_u32 s38, s34, 0xfff80080
	s_addc_u32 s39, s35, -1
	s_cmp_eq_u32 s77, 28
	s_cselect_b32 s45, s1, s39
	s_cselect_b32 s44, s29, s38
	s_cselect_b32 s43, s27, s47
	s_cselect_b32 s42, s41, s46
	s_add_i32 m0, s50, 0xc000
	s_branch .Lrot_P8_body

.Lrot_P8_body:
.LBB0_1649:
	ds_read_b128 v[130:133], v167
	ds_read_b128 v[134:137], v167 offset:1024
	ds_read_b128 v[138:141], v167 offset:2048
	ds_read_b128 v[142:145], v167 offset:3072
	ds_read_b128 v[168:171], v228
	ds_read_b128 v[172:175], v228 offset:1024
	ds_read_b128 v[176:179], v228 offset:2048
	ds_read_b128 v[180:183], v228 offset:3072
	ds_read_b128 v[184:187], v229
	ds_read_b128 v[188:191], v229 offset:1024
	ds_read_b128 v[192:195], v229 offset:2048
	ds_read_b128 v[196:199], v229 offset:3072
	ds_read_b128 v[200:203], v229 offset:4096
	ds_read_b128 v[204:207], v229 offset:5120
	ds_read_b128 v[208:211], v229 offset:6144
	ds_read_b128 v[212:215], v229 offset:7168
	global_load_lds_dwordx4 v158, s[34:35]
	s_add_i32 m0, s50, 0xe000
	s_nop 0
	global_load_lds_dwordx4 v160, s[34:35]
	s_waitcnt vmcnt(8)
	s_waitcnt lgkmcnt(0)
	s_barrier
	s_setprio 1
	s_waitcnt lgkmcnt(0)
	v_mfma_i32_16x16x64_i8 v[46:49], v[130:133], v[184:187], v[46:49]
	v_mfma_i32_16x16x64_i8 v[34:37], v[138:141], v[184:187], v[34:37]
	v_mfma_i32_16x16x64_i8 v[42:45], v[130:133], v[192:195], v[42:45]
	v_mfma_i32_16x16x64_i8 v[30:33], v[138:141], v[192:195], v[30:33]
	v_mfma_i32_16x16x64_i8 v[38:41], v[130:133], v[200:203], v[38:41]
	v_mfma_i32_16x16x64_i8 v[26:29], v[138:141], v[200:203], v[26:29]
	v_mfma_i32_16x16x64_i8 v[126:129], v[130:133], v[208:211], v[126:129]
	v_mfma_i32_16x16x64_i8 v[122:125], v[138:141], v[208:211], v[122:125]
	v_mfma_i32_16x16x64_i8 v[46:49], v[134:137], v[188:191], v[46:49]
	v_mfma_i32_16x16x64_i8 v[34:37], v[142:145], v[188:191], v[34:37]
	v_mfma_i32_16x16x64_i8 v[42:45], v[134:137], v[196:199], v[42:45]
	v_mfma_i32_16x16x64_i8 v[30:33], v[142:145], v[196:199], v[30:33]
	v_mfma_i32_16x16x64_i8 v[38:41], v[134:137], v[204:207], v[38:41]
	v_mfma_i32_16x16x64_i8 v[26:29], v[142:145], v[204:207], v[26:29]
	v_mfma_i32_16x16x64_i8 v[126:129], v[134:137], v[212:215], v[126:129]
	v_mfma_i32_16x16x64_i8 v[122:125], v[142:145], v[212:215], v[122:125]
	s_setprio 0
	s_setprio 1
	v_mfma_i32_16x16x64_i8 v[22:25], v[168:171], v[184:187], v[22:25]
	v_mfma_i32_16x16x64_i8 v[10:13], v[176:179], v[184:187], v[10:13]
	v_mfma_i32_16x16x64_i8 v[18:21], v[168:171], v[192:195], v[18:21]
	v_mfma_i32_16x16x64_i8 v[6:9], v[176:179], v[192:195], v[6:9]
	v_mfma_i32_16x16x64_i8 v[14:17], v[168:171], v[200:203], v[14:17]
	v_mfma_i32_16x16x64_i8 v[2:5], v[176:179], v[200:203], v[2:5]
	v_mfma_i32_16x16x64_i8 v[118:121], v[168:171], v[208:211], v[118:121]
	v_mfma_i32_16x16x64_i8 v[114:117], v[176:179], v[208:211], v[114:117]
	v_mfma_i32_16x16x64_i8 v[22:25], v[172:175], v[188:191], v[22:25]
	v_mfma_i32_16x16x64_i8 v[10:13], v[180:183], v[188:191], v[10:13]
	v_mfma_i32_16x16x64_i8 v[18:21], v[172:175], v[196:199], v[18:21]
	v_mfma_i32_16x16x64_i8 v[6:9], v[180:183], v[196:199], v[6:9]
	v_mfma_i32_16x16x64_i8 v[14:17], v[172:175], v[204:207], v[14:17]
	v_mfma_i32_16x16x64_i8 v[2:5], v[180:183], v[204:207], v[2:5]
	v_mfma_i32_16x16x64_i8 v[118:121], v[172:175], v[212:215], v[118:121]
	v_mfma_i32_16x16x64_i8 v[114:117], v[180:183], v[212:215], v[114:117]
	s_setprio 0
	s_add_u32 s98, s42, s14
	s_addc_u32 s99, s43, s15
	s_add_u32 s100, s44, s14
	s_addc_u32 s101, s45, s15
	s_add_i32 s38, s64, s49
	s_mov_b32 m0, s38
	s_barrier
	ds_read_b128 v[184:187], v229 offset:16384
	ds_read_b128 v[188:191], v229 offset:17408
	ds_read_b128 v[192:195], v229 offset:18432
	ds_read_b128 v[196:199], v229 offset:19456
	ds_read_b128 v[200:203], v229 offset:20480
	ds_read_b128 v[204:207], v229 offset:21504
	ds_read_b128 v[208:211], v229 offset:22528
	ds_read_b128 v[212:215], v229 offset:23552
	global_load_lds_dwordx4 v150, s[42:43]
	s_add_i32 m0, s38, 0x2000
	s_add_u32 s38, s42, 0x80000
	s_addc_u32 s39, s43, 0
	s_add_i32 s78, s65, s49
	global_load_lds_dwordx4 v154, s[42:43]
	s_mov_b32 m0, s78
	s_nop 0
	global_load_lds_dwordx4 v150, s[38:39]
	s_add_i32 m0, s78, 0x2000
	s_nop 0
	global_load_lds_dwordx4 v154, s[38:39]
	s_mov_b32 m0, s50
	s_nop 0
	global_load_lds_dwordx4 v148, s[44:45]
	s_mov_b32 m0, s51
	s_nop 0
	global_load_lds_dwordx4 v152, s[44:45]
	s_waitcnt vmcnt(8)
	s_waitcnt lgkmcnt(0)
	s_barrier
	s_setprio 1
	s_waitcnt lgkmcnt(0)
	v_mfma_i32_16x16x64_i8 v[94:97], v[130:133], v[184:187], v[94:97]
	v_mfma_i32_16x16x64_i8 v[70:73], v[138:141], v[184:187], v[70:73]
	v_mfma_i32_16x16x64_i8 v[86:89], v[130:133], v[192:195], v[86:89]
	v_mfma_i32_16x16x64_i8 v[62:65], v[138:141], v[192:195], v[62:65]
	v_mfma_i32_16x16x64_i8 v[78:81], v[130:133], v[200:203], v[78:81]
	v_mfma_i32_16x16x64_i8 v[54:57], v[138:141], v[200:203], v[54:57]
	v_mfma_i32_16x16x64_i8 v[110:113], v[130:133], v[208:211], v[110:113]
	v_mfma_i32_16x16x64_i8 v[106:109], v[138:141], v[208:211], v[106:109]
	v_mfma_i32_16x16x64_i8 v[94:97], v[134:137], v[188:191], v[94:97]
	v_mfma_i32_16x16x64_i8 v[70:73], v[142:145], v[188:191], v[70:73]
	v_mfma_i32_16x16x64_i8 v[86:89], v[134:137], v[196:199], v[86:89]
	v_mfma_i32_16x16x64_i8 v[62:65], v[142:145], v[196:199], v[62:65]
	v_mfma_i32_16x16x64_i8 v[78:81], v[134:137], v[204:207], v[78:81]
	v_mfma_i32_16x16x64_i8 v[54:57], v[142:145], v[204:207], v[54:57]
	v_mfma_i32_16x16x64_i8 v[110:113], v[134:137], v[212:215], v[110:113]
	v_mfma_i32_16x16x64_i8 v[106:109], v[142:145], v[212:215], v[106:109]
	s_setprio 0
	s_setprio 1
	v_mfma_i32_16x16x64_i8 v[90:93], v[168:171], v[184:187], v[90:93]
	v_mfma_i32_16x16x64_i8 v[66:69], v[176:179], v[184:187], v[66:69]
	v_mfma_i32_16x16x64_i8 v[82:85], v[168:171], v[192:195], v[82:85]
	v_mfma_i32_16x16x64_i8 v[58:61], v[176:179], v[192:195], v[58:61]
	v_mfma_i32_16x16x64_i8 v[74:77], v[168:171], v[200:203], v[74:77]
	v_mfma_i32_16x16x64_i8 v[50:53], v[176:179], v[200:203], v[50:53]
	v_mfma_i32_16x16x64_i8 v[102:105], v[168:171], v[208:211], v[102:105]
	v_mfma_i32_16x16x64_i8 v[98:101], v[176:179], v[208:211], v[98:101]
	v_mfma_i32_16x16x64_i8 v[90:93], v[172:175], v[188:191], v[90:93]
	v_mfma_i32_16x16x64_i8 v[66:69], v[180:183], v[188:191], v[66:69]
	v_mfma_i32_16x16x64_i8 v[82:85], v[172:175], v[196:199], v[82:85]
	v_mfma_i32_16x16x64_i8 v[58:61], v[180:183], v[196:199], v[58:61]
	v_mfma_i32_16x16x64_i8 v[74:77], v[172:175], v[204:207], v[74:77]
	v_mfma_i32_16x16x64_i8 v[50:53], v[180:183], v[204:207], v[50:53]
	v_mfma_i32_16x16x64_i8 v[102:105], v[172:175], v[212:215], v[102:105]
	v_mfma_i32_16x16x64_i8 v[98:101], v[180:183], v[212:215], v[98:101]
	s_setprio 0
	s_add_i32 s78, 0, 0x18000
	s_add_i32 s79, 0, 0x1c000
	s_add_u32 s38, s44, 0x80000
	s_addc_u32 s39, s45, 0
	s_mov_b32 m0, s52
	s_barrier
	v_add_u32_e32 v142, s78, v1
	v_add_u32_e32 v156, s79, v1
	ds_read_b128 v[130:133], v142
	ds_read_b128 v[134:137], v142 offset:1024
	ds_read_b128 v[138:141], v142 offset:2048
	ds_read_b128 v[142:145], v142 offset:3072
	ds_read_b128 v[168:171], v156
	ds_read_b128 v[172:175], v156 offset:1024
	ds_read_b128 v[176:179], v156 offset:2048
	ds_read_b128 v[180:183], v156 offset:3072
	ds_read_b128 v[184:187], v229 offset:32768
	ds_read_b128 v[188:191], v229 offset:33792
	ds_read_b128 v[192:195], v229 offset:34816
	ds_read_b128 v[196:199], v229 offset:35840
	ds_read_b128 v[200:203], v229 offset:36864
	ds_read_b128 v[204:207], v229 offset:37888
	ds_read_b128 v[208:211], v229 offset:38912
	ds_read_b128 v[212:215], v229 offset:39936
	global_load_lds_dwordx4 v148, s[38:39]
	s_mov_b32 m0, s53
	s_nop 0
	global_load_lds_dwordx4 v152, s[38:39]
	s_waitcnt vmcnt(8)
	s_waitcnt lgkmcnt(0)
	s_barrier
	s_setprio 1
	s_waitcnt lgkmcnt(0)
	v_mfma_i32_16x16x64_i8 v[46:49], v[130:133], v[184:187], v[46:49]
	v_mfma_i32_16x16x64_i8 v[34:37], v[138:141], v[184:187], v[34:37]
	v_mfma_i32_16x16x64_i8 v[42:45], v[130:133], v[192:195], v[42:45]
	v_mfma_i32_16x16x64_i8 v[30:33], v[138:141], v[192:195], v[30:33]
	v_mfma_i32_16x16x64_i8 v[38:41], v[130:133], v[200:203], v[38:41]
	v_mfma_i32_16x16x64_i8 v[26:29], v[138:141], v[200:203], v[26:29]
	v_mfma_i32_16x16x64_i8 v[126:129], v[130:133], v[208:211], v[126:129]
	v_mfma_i32_16x16x64_i8 v[122:125], v[138:141], v[208:211], v[122:125]
	v_mfma_i32_16x16x64_i8 v[46:49], v[134:137], v[188:191], v[46:49]
	v_mfma_i32_16x16x64_i8 v[34:37], v[142:145], v[188:191], v[34:37]
	v_mfma_i32_16x16x64_i8 v[42:45], v[134:137], v[196:199], v[42:45]
	v_mfma_i32_16x16x64_i8 v[30:33], v[142:145], v[196:199], v[30:33]
	v_mfma_i32_16x16x64_i8 v[38:41], v[134:137], v[204:207], v[38:41]
	v_mfma_i32_16x16x64_i8 v[26:29], v[142:145], v[204:207], v[26:29]
	v_mfma_i32_16x16x64_i8 v[126:129], v[134:137], v[212:215], v[126:129]
	v_mfma_i32_16x16x64_i8 v[122:125], v[142:145], v[212:215], v[122:125]
	s_setprio 0
	s_setprio 1
	v_mfma_i32_16x16x64_i8 v[22:25], v[168:171], v[184:187], v[22:25]
	v_mfma_i32_16x16x64_i8 v[10:13], v[176:179], v[184:187], v[10:13]
	v_mfma_i32_16x16x64_i8 v[18:21], v[168:171], v[192:195], v[18:21]
	v_mfma_i32_16x16x64_i8 v[6:9], v[176:179], v[192:195], v[6:9]
	v_mfma_i32_16x16x64_i8 v[14:17], v[168:171], v[200:203], v[14:17]
	v_mfma_i32_16x16x64_i8 v[2:5], v[176:179], v[200:203], v[2:5]
	v_mfma_i32_16x16x64_i8 v[118:121], v[168:171], v[208:211], v[118:121]
	v_mfma_i32_16x16x64_i8 v[114:117], v[176:179], v[208:211], v[114:117]
	v_mfma_i32_16x16x64_i8 v[22:25], v[172:175], v[188:191], v[22:25]
	v_mfma_i32_16x16x64_i8 v[10:13], v[180:183], v[188:191], v[10:13]
	v_mfma_i32_16x16x64_i8 v[18:21], v[172:175], v[196:199], v[18:21]
	v_mfma_i32_16x16x64_i8 v[6:9], v[180:183], v[196:199], v[6:9]
	v_mfma_i32_16x16x64_i8 v[14:17], v[172:175], v[204:207], v[14:17]
	v_mfma_i32_16x16x64_i8 v[2:5], v[180:183], v[204:207], v[2:5]
	v_mfma_i32_16x16x64_i8 v[118:121], v[172:175], v[212:215], v[118:121]
	v_mfma_i32_16x16x64_i8 v[114:117], v[180:183], v[212:215], v[114:117]
	s_setprio 0
	s_add_i32 s38, s78, s49
	s_mov_b32 m0, s38
	s_barrier
	ds_read_b128 v[184:187], v229 offset:49152
	ds_read_b128 v[188:191], v229 offset:50176
	ds_read_b128 v[192:195], v229 offset:51200
	ds_read_b128 v[196:199], v229 offset:52224
	ds_read_b128 v[200:203], v229 offset:53248
	ds_read_b128 v[204:207], v229 offset:54272
	ds_read_b128 v[208:211], v229 offset:55296
	ds_read_b128 v[212:215], v229 offset:56320
	global_load_lds_dwordx4 v150, s[98:99]
	s_add_i32 m0, s38, 0x2000
	s_add_u32 s38, s42, 0x80080
	s_addc_u32 s39, s43, 0
	s_add_i32 s42, s79, s49
	global_load_lds_dwordx4 v154, s[98:99]
	s_mov_b32 m0, s42
	s_nop 0
	global_load_lds_dwordx4 v150, s[38:39]
	s_add_i32 m0, s42, 0x2000
	s_nop 0
	global_load_lds_dwordx4 v154, s[38:39]
	s_mov_b32 m0, s57
	s_nop 0
	global_load_lds_dwordx4 v148, s[100:101]
	s_mov_b32 m0, s58
	s_nop 0
	global_load_lds_dwordx4 v152, s[100:101]
	s_waitcnt vmcnt(8)
	s_waitcnt lgkmcnt(0)
	s_barrier
	s_setprio 1
	s_waitcnt lgkmcnt(0)
	v_mfma_i32_16x16x64_i8 v[94:97], v[130:133], v[184:187], v[94:97]
	v_mfma_i32_16x16x64_i8 v[70:73], v[138:141], v[184:187], v[70:73]
	v_mfma_i32_16x16x64_i8 v[86:89], v[130:133], v[192:195], v[86:89]
	v_mfma_i32_16x16x64_i8 v[62:65], v[138:141], v[192:195], v[62:65]
	v_mfma_i32_16x16x64_i8 v[78:81], v[130:133], v[200:203], v[78:81]
	v_mfma_i32_16x16x64_i8 v[54:57], v[138:141], v[200:203], v[54:57]
	v_mfma_i32_16x16x64_i8 v[110:113], v[130:133], v[208:211], v[110:113]
	v_mfma_i32_16x16x64_i8 v[106:109], v[138:141], v[208:211], v[106:109]
	v_mfma_i32_16x16x64_i8 v[94:97], v[134:137], v[188:191], v[94:97]
	v_mfma_i32_16x16x64_i8 v[70:73], v[142:145], v[188:191], v[70:73]
	v_mfma_i32_16x16x64_i8 v[86:89], v[134:137], v[196:199], v[86:89]
	v_mfma_i32_16x16x64_i8 v[62:65], v[142:145], v[196:199], v[62:65]
	v_mfma_i32_16x16x64_i8 v[78:81], v[134:137], v[204:207], v[78:81]
	v_mfma_i32_16x16x64_i8 v[54:57], v[142:145], v[204:207], v[54:57]
	v_mfma_i32_16x16x64_i8 v[110:113], v[134:137], v[212:215], v[110:113]
	v_mfma_i32_16x16x64_i8 v[106:109], v[142:145], v[212:215], v[106:109]
	s_setprio 0
	s_setprio 1
	v_mfma_i32_16x16x64_i8 v[90:93], v[168:171], v[184:187], v[90:93]
	v_mfma_i32_16x16x64_i8 v[66:69], v[176:179], v[184:187], v[66:69]
	v_mfma_i32_16x16x64_i8 v[82:85], v[168:171], v[192:195], v[82:85]
	v_mfma_i32_16x16x64_i8 v[58:61], v[176:179], v[192:195], v[58:61]
	v_mfma_i32_16x16x64_i8 v[74:77], v[168:171], v[200:203], v[74:77]
	v_mfma_i32_16x16x64_i8 v[50:53], v[176:179], v[200:203], v[50:53]
	v_mfma_i32_16x16x64_i8 v[102:105], v[168:171], v[208:211], v[102:105]
	v_mfma_i32_16x16x64_i8 v[98:101], v[176:179], v[208:211], v[98:101]
	v_mfma_i32_16x16x64_i8 v[90:93], v[172:175], v[188:191], v[90:93]
	v_mfma_i32_16x16x64_i8 v[66:69], v[180:183], v[188:191], v[66:69]
	v_mfma_i32_16x16x64_i8 v[82:85], v[172:175], v[196:199], v[82:85]
	v_mfma_i32_16x16x64_i8 v[58:61], v[180:183], v[196:199], v[58:61]
	v_mfma_i32_16x16x64_i8 v[74:77], v[172:175], v[204:207], v[74:77]
	v_mfma_i32_16x16x64_i8 v[50:53], v[180:183], v[204:207], v[50:53]
	v_mfma_i32_16x16x64_i8 v[102:105], v[172:175], v[212:215], v[102:105]
	v_mfma_i32_16x16x64_i8 v[98:101], v[180:183], v[212:215], v[98:101]
	s_setprio 0
	s_add_i32 s77, s77, 2
	s_add_u32 s34, s34, 0x100
	s_addc_u32 s35, s35, 0
	s_add_u32 s46, s46, 0x100
	s_addc_u32 s47, s47, 0
	s_cmp_gt_u32 s77, 29
	s_cbranch_scc1 .Lrot_P8_exit
	s_add_u32 s38, s34, 0xfff80080
	s_addc_u32 s39, s35, -1
	s_cmp_eq_u32 s77, 28
	s_cselect_b32 s45, s1, s39
	s_cselect_b32 s44, s29, s38
	s_cselect_b32 s43, s27, s47
	s_cselect_b32 s42, s41, s46
	s_add_i32 m0, s50, 0xc000
	s_branch .Lrot_P8_head
.Lrot_P8_exit:
	s_barrier
	s_and_b64 vcc, exec, s[16:17]
	s_cbranch_vccz .LBB0_1652
	s_barrier

.LBB0_1898:
	s_add_u32 s20, s20, 0x158080
	s_addc_u32 s21, s21, 0
	s_add_u32 s47, s22, 0x100
	v_mov_b32_e32 v2, 0
	s_addc_u32 s48, s23, 0
	s_mov_b32 s49, -2
	v_mov_b32_e32 v3, v2
	v_mov_b32_e32 v4, v2
	v_mov_b32_e32 v5, v2
	v_mov_b32_e32 v6, v2
	v_mov_b32_e32 v7, v2
	v_mov_b32_e32 v8, v2
	v_mov_b32_e32 v9, v2
	v_mov_b32_e32 v18, v2
	v_mov_b32_e32 v19, v2
	v_mov_b32_e32 v20, v2
	v_mov_b32_e32 v21, v2
	v_mov_b32_e32 v22, v2
	v_mov_b32_e32 v23, v2
	v_mov_b32_e32 v24, v2
	v_mov_b32_e32 v25, v2
	v_mov_b32_e32 v34, v2
	v_mov_b32_e32 v35, v2
	v_mov_b32_e32 v36, v2
	v_mov_b32_e32 v37, v2
	v_mov_b32_e32 v38, v2
	v_mov_b32_e32 v39, v2
	v_mov_b32_e32 v40, v2
	v_mov_b32_e32 v41, v2
	v_mov_b32_e32 v50, v2
	v_mov_b32_e32 v51, v2
	v_mov_b32_e32 v52, v2
	v_mov_b32_e32 v53, v2
	v_mov_b32_e32 v54, v2
	v_mov_b32_e32 v55, v2
	v_mov_b32_e32 v56, v2
	v_mov_b32_e32 v57, v2
	v_mov_b32_e32 v10, v2
	v_mov_b32_e32 v11, v2
	v_mov_b32_e32 v12, v2
	v_mov_b32_e32 v13, v2
	v_mov_b32_e32 v14, v2
	v_mov_b32_e32 v15, v2
	v_mov_b32_e32 v16, v2
	v_mov_b32_e32 v17, v2
	v_mov_b32_e32 v26, v2
	v_mov_b32_e32 v27, v2
	v_mov_b32_e32 v28, v2
	v_mov_b32_e32 v29, v2
	v_mov_b32_e32 v30, v2
	v_mov_b32_e32 v31, v2
	v_mov_b32_e32 v32, v2
	v_mov_b32_e32 v33, v2
	v_mov_b32_e32 v42, v2
	v_mov_b32_e32 v43, v2
	v_mov_b32_e32 v44, v2
	v_mov_b32_e32 v45, v2
	v_mov_b32_e32 v46, v2
	v_mov_b32_e32 v47, v2
	v_mov_b32_e32 v48, v2
	v_mov_b32_e32 v49, v2
	v_mov_b32_e32 v58, v2
	v_mov_b32_e32 v59, v2
	v_mov_b32_e32 v60, v2
	v_mov_b32_e32 v61, v2
	v_mov_b32_e32 v62, v2
	v_mov_b32_e32 v63, v2
	v_mov_b32_e32 v64, v2
	v_mov_b32_e32 v65, v2
	v_mov_b32_e32 v66, v2
	v_mov_b32_e32 v67, v2
	v_mov_b32_e32 v68, v2
	v_mov_b32_e32 v69, v2
	v_mov_b32_e32 v70, v2
	v_mov_b32_e32 v71, v2
	v_mov_b32_e32 v72, v2
	v_mov_b32_e32 v73, v2
	v_mov_b32_e32 v82, v2
	v_mov_b32_e32 v83, v2
	v_mov_b32_e32 v84, v2
	v_mov_b32_e32 v85, v2
	v_mov_b32_e32 v86, v2
	v_mov_b32_e32 v87, v2
	v_mov_b32_e32 v88, v2
	v_mov_b32_e32 v89, v2
	v_mov_b32_e32 v98, v2
	v_mov_b32_e32 v99, v2
	v_mov_b32_e32 v100, v2
	v_mov_b32_e32 v101, v2
	v_mov_b32_e32 v102, v2
	v_mov_b32_e32 v103, v2
	v_mov_b32_e32 v104, v2
	v_mov_b32_e32 v105, v2
	v_mov_b32_e32 v114, v2
	v_mov_b32_e32 v115, v2
	v_mov_b32_e32 v116, v2
	v_mov_b32_e32 v117, v2
	v_mov_b32_e32 v118, v2
	v_mov_b32_e32 v119, v2
	v_mov_b32_e32 v120, v2
	v_mov_b32_e32 v121, v2
	v_mov_b32_e32 v74, v2
	v_mov_b32_e32 v75, v2
	v_mov_b32_e32 v76, v2
	v_mov_b32_e32 v77, v2
	v_mov_b32_e32 v78, v2
	v_mov_b32_e32 v79, v2
	v_mov_b32_e32 v80, v2
	v_mov_b32_e32 v81, v2
	v_mov_b32_e32 v90, v2
	v_mov_b32_e32 v91, v2
	v_mov_b32_e32 v92, v2
	v_mov_b32_e32 v93, v2
	v_mov_b32_e32 v94, v2
	v_mov_b32_e32 v95, v2
	v_mov_b32_e32 v96, v2
	v_mov_b32_e32 v97, v2
	v_mov_b32_e32 v106, v2
	v_mov_b32_e32 v107, v2
	v_mov_b32_e32 v108, v2
	v_mov_b32_e32 v109, v2
	v_mov_b32_e32 v110, v2
	v_mov_b32_e32 v111, v2
	v_mov_b32_e32 v112, v2
	v_mov_b32_e32 v113, v2
	v_mov_b32_e32 v138, v2
	v_mov_b32_e32 v139, v2
	v_mov_b32_e32 v140, v2
	v_mov_b32_e32 v141, v2
	v_mov_b32_e32 v142, v2
	v_mov_b32_e32 v143, v2
	v_mov_b32_e32 v144, v2
	v_mov_b32_e32 v145, v2
	s_add_u32 s22, s20, 0xffea8080
	s_addc_u32 s23, s21, -1
	s_branch .Lrot_P10_body

.Lrot_P10_body:
.LBB0_1899:
	ds_read_b128 v[122:125], v169
	ds_read_b128 v[126:129], v169 offset:1024
	ds_read_b128 v[130:133], v169 offset:2048
	ds_read_b128 v[134:137], v169 offset:3072
	ds_read_b128 v[172:175], v170
	ds_read_b128 v[176:179], v170 offset:1024
	ds_read_b128 v[180:183], v170 offset:2048
	ds_read_b128 v[184:187], v170 offset:3072
	s_cmpk_eq_i32 s49, 0x52
	s_cselect_b32 s25, s5, s23
	s_cselect_b32 s24, s4, s22
	s_cselect_b32 s23, s19, s48
	s_cselect_b32 s22, s18, s47
	s_add_i32 m0, s30, 0xc000
	ds_read_b128 v[188:191], v171
	ds_read_b128 v[192:195], v171 offset:1024
	ds_read_b128 v[196:199], v171 offset:2048
	ds_read_b128 v[200:203], v171 offset:3072
	ds_read_b128 v[204:207], v171 offset:4096
	ds_read_b128 v[208:211], v171 offset:5120
	ds_read_b128 v[212:215], v171 offset:6144
	ds_read_b128 v[216:219], v171 offset:7168
	global_load_lds_dwordx4 v156, s[20:21]
	s_add_i32 m0, s30, 0xe000
	s_nop 0
	global_load_lds_dwordx4 v158, s[20:21]
	s_waitcnt vmcnt(8)
	s_waitcnt lgkmcnt(0)
	s_barrier
	s_setprio 1
	s_waitcnt lgkmcnt(0)
	v_mfma_i32_16x16x64_i8 v[142:145], v[122:125], v[188:191], v[142:145]
	v_mfma_i32_16x16x64_i8 v[138:141], v[130:133], v[188:191], v[138:141]
	v_mfma_i32_16x16x64_i8 v[110:113], v[122:125], v[196:199], v[110:113]
	v_mfma_i32_16x16x64_i8 v[106:109], v[130:133], v[196:199], v[106:109]
	v_mfma_i32_16x16x64_i8 v[94:97], v[122:125], v[204:207], v[94:97]
	v_mfma_i32_16x16x64_i8 v[90:93], v[130:133], v[204:207], v[90:93]
	v_mfma_i32_16x16x64_i8 v[78:81], v[122:125], v[212:215], v[78:81]
	v_mfma_i32_16x16x64_i8 v[74:77], v[130:133], v[212:215], v[74:77]
	v_mfma_i32_16x16x64_i8 v[142:145], v[126:129], v[192:195], v[142:145]
	v_mfma_i32_16x16x64_i8 v[138:141], v[134:137], v[192:195], v[138:141]
	v_mfma_i32_16x16x64_i8 v[110:113], v[126:129], v[200:203], v[110:113]
	v_mfma_i32_16x16x64_i8 v[106:109], v[134:137], v[200:203], v[106:109]
	v_mfma_i32_16x16x64_i8 v[94:97], v[126:129], v[208:211], v[94:97]
	v_mfma_i32_16x16x64_i8 v[90:93], v[134:137], v[208:211], v[90:93]
	v_mfma_i32_16x16x64_i8 v[78:81], v[126:129], v[216:219], v[78:81]
	v_mfma_i32_16x16x64_i8 v[74:77], v[134:137], v[216:219], v[74:77]
	s_setprio 0
	s_setprio 1
	v_mfma_i32_16x16x64_i8 v[118:121], v[172:175], v[188:191], v[118:121]
	v_mfma_i32_16x16x64_i8 v[114:117], v[180:183], v[188:191], v[114:117]
	v_mfma_i32_16x16x64_i8 v[102:105], v[172:175], v[196:199], v[102:105]
	v_mfma_i32_16x16x64_i8 v[98:101], v[180:183], v[196:199], v[98:101]
	v_mfma_i32_16x16x64_i8 v[86:89], v[172:175], v[204:207], v[86:89]
	v_mfma_i32_16x16x64_i8 v[82:85], v[180:183], v[204:207], v[82:85]
	v_mfma_i32_16x16x64_i8 v[70:73], v[172:175], v[212:215], v[70:73]
	v_mfma_i32_16x16x64_i8 v[66:69], v[180:183], v[212:215], v[66:69]
	v_mfma_i32_16x16x64_i8 v[118:121], v[176:179], v[192:195], v[118:121]
	v_mfma_i32_16x16x64_i8 v[114:117], v[184:187], v[192:195], v[114:117]
	v_mfma_i32_16x16x64_i8 v[102:105], v[176:179], v[200:203], v[102:105]
	v_mfma_i32_16x16x64_i8 v[98:101], v[184:187], v[200:203], v[98:101]
	v_mfma_i32_16x16x64_i8 v[86:89], v[176:179], v[208:211], v[86:89]
	v_mfma_i32_16x16x64_i8 v[82:85], v[184:187], v[208:211], v[82:85]
	v_mfma_i32_16x16x64_i8 v[70:73], v[176:179], v[216:219], v[70:73]
	v_mfma_i32_16x16x64_i8 v[66:69], v[184:187], v[216:219], v[66:69]
	s_setprio 0
	s_add_u32 s98, s22, s14
	s_addc_u32 s99, s23, s15
	s_add_u32 s100, s24, s14
	s_addc_u32 s101, s25, s15
	s_add_i32 s38, s41, s29
	s_mov_b32 m0, s38
	s_barrier
	ds_read_b128 v[188:191], v171 offset:16384
	ds_read_b128 v[192:195], v171 offset:17408
	ds_read_b128 v[196:199], v171 offset:18432
	ds_read_b128 v[200:203], v171 offset:19456
	ds_read_b128 v[204:207], v171 offset:20480
	ds_read_b128 v[208:211], v171 offset:21504
	ds_read_b128 v[212:215], v171 offset:22528
	ds_read_b128 v[216:219], v171 offset:23552
	global_load_lds_dwordx4 v148, s[22:23]
	s_add_i32 m0, s38, 0x2000
	s_add_u32 s38, s22, 0x158000
	s_addc_u32 s39, s23, 0
	s_add_i32 s50, s42, s29
	global_load_lds_dwordx4 v152, s[22:23]
	s_mov_b32 m0, s50
	s_nop 0
	global_load_lds_dwordx4 v148, s[38:39]
	s_add_i32 m0, s50, 0x2000
	s_nop 0
	global_load_lds_dwordx4 v152, s[38:39]
	s_mov_b32 m0, s30
	s_nop 0
	global_load_lds_dwordx4 v146, s[24:25]
	s_mov_b32 m0, s31
	s_nop 0
	global_load_lds_dwordx4 v150, s[24:25]
	s_waitcnt vmcnt(8)
	s_waitcnt lgkmcnt(0)
	s_barrier
	s_setprio 1
	s_waitcnt lgkmcnt(0)
	v_mfma_i32_16x16x64_i8 v[62:65], v[122:125], v[188:191], v[62:65]
	v_mfma_i32_16x16x64_i8 v[58:61], v[130:133], v[188:191], v[58:61]
	v_mfma_i32_16x16x64_i8 v[46:49], v[122:125], v[196:199], v[46:49]
	v_mfma_i32_16x16x64_i8 v[42:45], v[130:133], v[196:199], v[42:45]
	v_mfma_i32_16x16x64_i8 v[30:33], v[122:125], v[204:207], v[30:33]
	v_mfma_i32_16x16x64_i8 v[26:29], v[130:133], v[204:207], v[26:29]
	v_mfma_i32_16x16x64_i8 v[14:17], v[122:125], v[212:215], v[14:17]
	v_mfma_i32_16x16x64_i8 v[10:13], v[130:133], v[212:215], v[10:13]
	v_mfma_i32_16x16x64_i8 v[62:65], v[126:129], v[192:195], v[62:65]
	v_mfma_i32_16x16x64_i8 v[58:61], v[134:137], v[192:195], v[58:61]
	v_mfma_i32_16x16x64_i8 v[46:49], v[126:129], v[200:203], v[46:49]
	v_mfma_i32_16x16x64_i8 v[42:45], v[134:137], v[200:203], v[42:45]
	v_mfma_i32_16x16x64_i8 v[30:33], v[126:129], v[208:211], v[30:33]
	v_mfma_i32_16x16x64_i8 v[26:29], v[134:137], v[208:211], v[26:29]
	v_mfma_i32_16x16x64_i8 v[14:17], v[126:129], v[216:219], v[14:17]
	v_mfma_i32_16x16x64_i8 v[10:13], v[134:137], v[216:219], v[10:13]
	s_setprio 0
	s_setprio 1
	v_mfma_i32_16x16x64_i8 v[54:57], v[172:175], v[188:191], v[54:57]
	v_mfma_i32_16x16x64_i8 v[50:53], v[180:183], v[188:191], v[50:53]
	v_mfma_i32_16x16x64_i8 v[38:41], v[172:175], v[196:199], v[38:41]
	v_mfma_i32_16x16x64_i8 v[34:37], v[180:183], v[196:199], v[34:37]
	v_mfma_i32_16x16x64_i8 v[22:25], v[172:175], v[204:207], v[22:25]
	v_mfma_i32_16x16x64_i8 v[18:21], v[180:183], v[204:207], v[18:21]
	v_mfma_i32_16x16x64_i8 v[6:9], v[172:175], v[212:215], v[6:9]
	v_mfma_i32_16x16x64_i8 v[2:5], v[180:183], v[212:215], v[2:5]
	v_mfma_i32_16x16x64_i8 v[54:57], v[176:179], v[192:195], v[54:57]
	v_mfma_i32_16x16x64_i8 v[50:53], v[184:187], v[192:195], v[50:53]
	v_mfma_i32_16x16x64_i8 v[38:41], v[176:179], v[200:203], v[38:41]
	v_mfma_i32_16x16x64_i8 v[34:37], v[184:187], v[200:203], v[34:37]
	v_mfma_i32_16x16x64_i8 v[22:25], v[176:179], v[208:211], v[22:25]
	v_mfma_i32_16x16x64_i8 v[18:21], v[184:187], v[208:211], v[18:21]
	v_mfma_i32_16x16x64_i8 v[6:9], v[176:179], v[216:219], v[6:9]
	v_mfma_i32_16x16x64_i8 v[2:5], v[184:187], v[216:219], v[2:5]
	s_setprio 0
	s_add_i32 s38, 0, 0x18000
	s_add_i32 s39, 0, 0x1c000
	s_add_u32 s24, s24, 0x158000
	s_addc_u32 s25, s25, 0
	s_mov_b32 m0, s33
	s_barrier
	v_add_u32_e32 v134, s38, v167
	v_add_u32_e32 v154, s39, v167
	ds_read_b128 v[122:125], v134
	ds_read_b128 v[126:129], v134 offset:1024
	ds_read_b128 v[130:133], v134 offset:2048
	ds_read_b128 v[134:137], v134 offset:3072
	ds_read_b128 v[172:175], v154
	ds_read_b128 v[176:179], v154 offset:1024
	ds_read_b128 v[180:183], v154 offset:2048
	ds_read_b128 v[184:187], v154 offset:3072
	ds_read_b128 v[188:191], v171 offset:32768
	ds_read_b128 v[192:195], v171 offset:33792
	ds_read_b128 v[196:199], v171 offset:34816
	ds_read_b128 v[200:203], v171 offset:35840
	ds_read_b128 v[204:207], v171 offset:36864
	ds_read_b128 v[208:211], v171 offset:37888
	ds_read_b128 v[212:215], v171 offset:38912
	ds_read_b128 v[216:219], v171 offset:39936
	global_load_lds_dwordx4 v146, s[24:25]
	s_mov_b32 m0, s34
	s_nop 0
	global_load_lds_dwordx4 v150, s[24:25]
	s_waitcnt vmcnt(8)
	s_waitcnt lgkmcnt(0)
	s_barrier
	s_setprio 1
	s_waitcnt lgkmcnt(0)
	v_mfma_i32_16x16x64_i8 v[142:145], v[122:125], v[188:191], v[142:145]
	v_mfma_i32_16x16x64_i8 v[138:141], v[130:133], v[188:191], v[138:141]
	v_mfma_i32_16x16x64_i8 v[110:113], v[122:125], v[196:199], v[110:113]
	v_mfma_i32_16x16x64_i8 v[106:109], v[130:133], v[196:199], v[106:109]
	v_mfma_i32_16x16x64_i8 v[94:97], v[122:125], v[204:207], v[94:97]
	v_mfma_i32_16x16x64_i8 v[90:93], v[130:133], v[204:207], v[90:93]
	v_mfma_i32_16x16x64_i8 v[78:81], v[122:125], v[212:215], v[78:81]
	v_mfma_i32_16x16x64_i8 v[74:77], v[130:133], v[212:215], v[74:77]
	v_mfma_i32_16x16x64_i8 v[142:145], v[126:129], v[192:195], v[142:145]
	v_mfma_i32_16x16x64_i8 v[138:141], v[134:137], v[192:195], v[138:141]
	v_mfma_i32_16x16x64_i8 v[110:113], v[126:129], v[200:203], v[110:113]
	v_mfma_i32_16x16x64_i8 v[106:109], v[134:137], v[200:203], v[106:109]
	v_mfma_i32_16x16x64_i8 v[94:97], v[126:129], v[208:211], v[94:97]
	v_mfma_i32_16x16x64_i8 v[90:93], v[134:137], v[208:211], v[90:93]
	v_mfma_i32_16x16x64_i8 v[78:81], v[126:129], v[216:219], v[78:81]
	v_mfma_i32_16x16x64_i8 v[74:77], v[134:137], v[216:219], v[74:77]
	s_setprio 0
	s_setprio 1
	v_mfma_i32_16x16x64_i8 v[118:121], v[172:175], v[188:191], v[118:121]
	v_mfma_i32_16x16x64_i8 v[114:117], v[180:183], v[188:191], v[114:117]
	v_mfma_i32_16x16x64_i8 v[102:105], v[172:175], v[196:199], v[102:105]
	v_mfma_i32_16x16x64_i8 v[98:101], v[180:183], v[196:199], v[98:101]
	v_mfma_i32_16x16x64_i8 v[86:89], v[172:175], v[204:207], v[86:89]
	v_mfma_i32_16x16x64_i8 v[82:85], v[180:183], v[204:207], v[82:85]
	v_mfma_i32_16x16x64_i8 v[70:73], v[172:175], v[212:215], v[70:73]
	v_mfma_i32_16x16x64_i8 v[66:69], v[180:183], v[212:215], v[66:69]
	v_mfma_i32_16x16x64_i8 v[118:121], v[176:179], v[192:195], v[118:121]
	v_mfma_i32_16x16x64_i8 v[114:117], v[184:187], v[192:195], v[114:117]
	v_mfma_i32_16x16x64_i8 v[102:105], v[176:179], v[200:203], v[102:105]
	v_mfma_i32_16x16x64_i8 v[98:101], v[184:187], v[200:203], v[98:101]
	v_mfma_i32_16x16x64_i8 v[86:89], v[176:179], v[208:211], v[86:89]
	v_mfma_i32_16x16x64_i8 v[82:85], v[184:187], v[208:211], v[82:85]
	v_mfma_i32_16x16x64_i8 v[70:73], v[176:179], v[216:219], v[70:73]
	v_mfma_i32_16x16x64_i8 v[66:69], v[184:187], v[216:219], v[66:69]
	s_setprio 0
	s_add_i32 s24, s38, s29
	s_mov_b32 m0, s24
	s_barrier
	ds_read_b128 v[188:191], v171 offset:49152
	ds_read_b128 v[192:195], v171 offset:50176
	ds_read_b128 v[196:199], v171 offset:51200
	ds_read_b128 v[200:203], v171 offset:52224
	ds_read_b128 v[204:207], v171 offset:53248
	ds_read_b128 v[208:211], v171 offset:54272
	ds_read_b128 v[212:215], v171 offset:55296
	ds_read_b128 v[216:219], v171 offset:56320
	global_load_lds_dwordx4 v148, s[98:99]
	s_add_i32 m0, s24, 0x2000
	s_add_u32 s22, s22, 0x158080
	s_addc_u32 s23, s23, 0
	s_add_i32 s24, s39, s29
	global_load_lds_dwordx4 v152, s[98:99]
	s_mov_b32 m0, s24
	s_nop 0
	global_load_lds_dwordx4 v148, s[22:23]
	s_add_i32 m0, s24, 0x2000
	s_nop 0
	global_load_lds_dwordx4 v152, s[22:23]
	s_mov_b32 m0, s36
	s_nop 0
	global_load_lds_dwordx4 v146, s[100:101]
	s_mov_b32 m0, s37
	s_nop 0
	global_load_lds_dwordx4 v150, s[100:101]
	s_waitcnt vmcnt(8)
	s_waitcnt lgkmcnt(0)
	s_barrier
	s_setprio 1
	s_waitcnt lgkmcnt(0)
	v_mfma_i32_16x16x64_i8 v[62:65], v[122:125], v[188:191], v[62:65]
	v_mfma_i32_16x16x64_i8 v[58:61], v[130:133], v[188:191], v[58:61]
	v_mfma_i32_16x16x64_i8 v[46:49], v[122:125], v[196:199], v[46:49]
	v_mfma_i32_16x16x64_i8 v[42:45], v[130:133], v[196:199], v[42:45]
	v_mfma_i32_16x16x64_i8 v[30:33], v[122:125], v[204:207], v[30:33]
	v_mfma_i32_16x16x64_i8 v[26:29], v[130:133], v[204:207], v[26:29]
	v_mfma_i32_16x16x64_i8 v[14:17], v[122:125], v[212:215], v[14:17]
	v_mfma_i32_16x16x64_i8 v[10:13], v[130:133], v[212:215], v[10:13]
	v_mfma_i32_16x16x64_i8 v[62:65], v[126:129], v[192:195], v[62:65]
	v_mfma_i32_16x16x64_i8 v[58:61], v[134:137], v[192:195], v[58:61]
	v_mfma_i32_16x16x64_i8 v[46:49], v[126:129], v[200:203], v[46:49]
	v_mfma_i32_16x16x64_i8 v[42:45], v[134:137], v[200:203], v[42:45]
	v_mfma_i32_16x16x64_i8 v[30:33], v[126:129], v[208:211], v[30:33]
	v_mfma_i32_16x16x64_i8 v[26:29], v[134:137], v[208:211], v[26:29]
	v_mfma_i32_16x16x64_i8 v[14:17], v[126:129], v[216:219], v[14:17]
	v_mfma_i32_16x16x64_i8 v[10:13], v[134:137], v[216:219], v[10:13]
	s_setprio 0
	s_setprio 1
	v_mfma_i32_16x16x64_i8 v[54:57], v[172:175], v[188:191], v[54:57]
	v_mfma_i32_16x16x64_i8 v[50:53], v[180:183], v[188:191], v[50:53]
	v_mfma_i32_16x16x64_i8 v[38:41], v[172:175], v[196:199], v[38:41]
	v_mfma_i32_16x16x64_i8 v[34:37], v[180:183], v[196:199], v[34:37]
	v_mfma_i32_16x16x64_i8 v[22:25], v[172:175], v[204:207], v[22:25]
	v_mfma_i32_16x16x64_i8 v[18:21], v[180:183], v[204:207], v[18:21]
	v_mfma_i32_16x16x64_i8 v[6:9], v[172:175], v[212:215], v[6:9]
	v_mfma_i32_16x16x64_i8 v[2:5], v[180:183], v[212:215], v[2:5]
	v_mfma_i32_16x16x64_i8 v[54:57], v[176:179], v[192:195], v[54:57]
	v_mfma_i32_16x16x64_i8 v[50:53], v[184:187], v[192:195], v[50:53]
	v_mfma_i32_16x16x64_i8 v[38:41], v[176:179], v[200:203], v[38:41]
	v_mfma_i32_16x16x64_i8 v[34:37], v[184:187], v[200:203], v[34:37]
	v_mfma_i32_16x16x64_i8 v[22:25], v[176:179], v[208:211], v[22:25]
	v_mfma_i32_16x16x64_i8 v[18:21], v[184:187], v[208:211], v[18:21]
	v_mfma_i32_16x16x64_i8 v[6:9], v[176:179], v[216:219], v[6:9]
	v_mfma_i32_16x16x64_i8 v[2:5], v[184:187], v[216:219], v[2:5]
	s_setprio 0
	s_add_i32 s49, s49, 2
	s_add_u32 s20, s20, 0x100
	s_addc_u32 s21, s21, 0
	s_add_u32 s47, s47, 0x100
	s_addc_u32 s48, s48, 0
	s_cmpk_gt_u32 s49, 0x53
	s_cbranch_scc1 .Lrot_P10_exit
	s_add_u32 s22, s20, 0xffea8080
	s_addc_u32 s23, s21, -1
	s_branch .Lrot_P10_head
